# speedup vs baseline: 1.0188x; 1.0188x over previous
_Z12k1_colsum_q8PKfPjPfS2_:
	s_load_dwordx8 s[4:11], s[0:1], 0x0
	v_and_b32_e32 v1, 63, v0
	v_lshrrev_b32_e32 v41, 6, v0
	s_mul_i32 s12, s2, 0xc35
	s_lshr_b32 s12, s12, 4
	v_readfirstlane_b32 s14, v41
	s_add_i32 s13, s2, 1
	s_mul_i32 s13, s13, 0xc35
	s_lshr_b32 s13, s13, 4
	s_sub_u32 s13, s13, s12
	s_sub_u32 s15, s13, 0xc0
	s_cmp_lt_u32 s14, s15
	s_cselect_b32 s29, 1, 0
	v_lshlrev_b32_e32 v34, 4, v1
	v_min_u32_e32 v35, 57, v1
	v_lshlrev_b32_e32 v35, 4, v35
	v_cmp_gt_u32_e64 s[18:19], 58, v1
	s_lshl_b32 s35, s14, 13
	s_add_u32 s36, s35, 0x1000
	v_add_u32_e32 v38, s35, v34
	v_lshrrev_b32_e32 v41, 5, v1
	v_mov_b32_e32 v42, 0xc35000
	v_mul_lo_u32 v39, v41, v42
	v_and_b32_e32 v42, 31, v1
	v_lshl_add_u32 v39, v42, 2, v39
	v_mov_b32_e32 v2, 0
	v_mov_b32_e32 v3, 0
	v_mov_b32_e32 v4, 0
	v_mov_b32_e32 v5, 0
	v_mov_b32_e32 v6, 0
	v_mov_b32_e32 v7, 0
	v_mov_b32_e32 v8, 0
	v_mov_b32_e32 v9, 0
	v_mov_b32_e32 v10, 0
	v_mov_b32_e32 v11, 0
	v_mov_b32_e32 v12, 0
	v_mov_b32_e32 v13, 0
	v_mov_b32_e32 v14, 0
	v_mov_b32_e32 v15, 0
	v_mov_b32_e32 v16, 0
	v_mov_b32_e32 v17, 0
	v_mov_b32_e32 v40, 0
	v_mov_b32_e32 v47, 0x42fe0000
	s_mov_b32 s32, 0x42fe0000
	s_mov_b32 s33, 0xc0c0400
	s_mov_b32 s34, 0x4000c0c
	s_add_u32 s15, s12, s14
	s_mul_i32 s37, s15, 0xfa0
	s_lshl_b32 s15, s15, 7
	s_waitcnt lgkmcnt(0)
	s_add_u32 s16, s4, s37
	s_addc_u32 s17, s5, 0
	s_add_u32 s40, s6, s15
	s_addc_u32 s41, s7, 0
	s_add_u32 s20, s40, 0
	s_addc_u32 s21, s41, 0
	s_add_u32 s22, s20, 0x186a000
	s_addc_u32 s23, s21, 0
	s_add_u32 s24, s22, 0x186a000
	s_addc_u32 s25, s23, 0
	s_add_u32 s26, s24, 0x186a000
	s_addc_u32 s27, s25, 0
	s_mov_b32 m0, s35
	s_nop 0
	global_load_lds_dwordx4 v34, s[16:17] nt
	global_load_lds_dwordx4 v34, s[16:17] offset:1024 nt
	global_load_lds_dwordx4 v34, s[16:17] offset:2048 nt
	global_load_lds_dwordx4 v35, s[16:17] offset:3072 nt
	s_add_u32 s16, s16, 0x7d00
	s_addc_u32 s17, s17, 0
	s_mov_b32 m0, s36
	s_nop 0
	global_load_lds_dwordx4 v34, s[16:17] nt
	global_load_lds_dwordx4 v34, s[16:17] offset:1024 nt
	global_load_lds_dwordx4 v34, s[16:17] offset:2048 nt
	global_load_lds_dwordx4 v35, s[16:17] offset:3072 nt
	s_add_u32 s16, s16, 0x7d00
	s_addc_u32 s17, s17, 0
	s_waitcnt vmcnt(4)
	ds_read_b128 v[18:21], v38 offset:0
	ds_read_b128 v[22:25], v38 offset:1024
	ds_read_b128 v[26:29], v38 offset:2048
	ds_read_b128 v[30:33], v38 offset:3072
	s_waitcnt lgkmcnt(0)
	s_mov_b32 m0, s35
	s_nop 0
	global_load_lds_dwordx4 v34, s[16:17] nt
	global_load_lds_dwordx4 v34, s[16:17] offset:1024 nt
	global_load_lds_dwordx4 v34, s[16:17] offset:2048 nt
	global_load_lds_dwordx4 v35, s[16:17] offset:3072 nt
	s_add_u32 s16, s16, 0x7d00
	s_addc_u32 s17, s17, 0
	v_cndmask_b32_e64 v30, 0, v30, s[18:19]
	v_cndmask_b32_e64 v31, 0, v31, s[18:19]
	v_cndmask_b32_e64 v32, 0, v32, s[18:19]
	v_cndmask_b32_e64 v33, 0, v33, s[18:19]
	v_max3_f32 v41, |v18|, |v19|, |v20|
	v_max3_f32 v42, |v21|, |v22|, |v23|
	v_max3_f32 v43, |v24|, |v25|, |v26|
	v_max3_f32 v44, |v27|, |v28|, |v29|
	v_max3_f32 v48, |v30|, |v31|, |v32|
	v_max3_f32 v41, v41, v42, |v33|
	v_max3_f32 v43, v43, v44, v48
	v_max_f32_e32 v41, v41, v43
	v_pk_add_f32 v[2:3], v[2:3], v[18:19]
	v_pk_add_f32 v[4:5], v[4:5], v[20:21]
	v_max_f32_dpp v41, v41, v41 quad_perm:[1,0,3,2] row_mask:0xf bank_mask:0xf
	v_pk_add_f32 v[6:7], v[6:7], v[22:23]
	v_pk_add_f32 v[8:9], v[8:9], v[24:25]
	v_max_f32_dpp v41, v41, v41 quad_perm:[2,3,0,1] row_mask:0xf bank_mask:0xf
	v_pk_add_f32 v[10:11], v[10:11], v[26:27]
	v_pk_add_f32 v[12:13], v[12:13], v[28:29]
	v_max_f32_dpp v41, v41, v41 row_half_mirror row_mask:0xf bank_mask:0xf
	v_pk_add_f32 v[14:15], v[14:15], v[30:31]
	v_pk_add_f32 v[16:17], v[16:17], v[32:33]
	v_max_f32_dpp v41, v41, v41 row_mirror row_mask:0xf bank_mask:0xf
	s_nop 1
	v_max_f32_dpp v41, v41, v41 row_bcast:15 row_mask:0xa bank_mask:0xf
	s_nop 1
	v_max_f32_dpp v41, v41, v41 row_bcast:31 row_mask:0xc bank_mask:0xf
	s_nop 1
	v_readlane_b32 s28, v41, 63
	s_nop 1
	v_div_scale_f32 v48, s[30:31], s28, s28, v47
	v_rcp_f32_e32 v49, v48
	s_nop 0
	v_fma_f32 v50, -v48, v49, 1.0
	v_fmac_f32_e32 v49, v50, v49
	v_mov_b32_e32 v50, s28
	v_div_scale_f32 v50, vcc, s32, v50, s32
	v_mul_f32_e32 v51, v50, v49
	v_fma_f32 v52, -v48, v51, v50
	v_fmac_f32_e32 v51, v52, v49
	v_fma_f32 v48, -v48, v51, v50
	v_div_fmas_f32 v48, v48, v49, v51
	v_div_fixup_f32 v48, v48, s28, v47
	v_cmp_gt_f32_e64 vcc, s28, 0
	v_writelane_b32 v40, s28, 0
	s_nop 0
	v_cndmask_b32_e32 v48, 0, v48, vcc
	v_fmaak_f32 v49, v18, v48, 0x4b400000
	v_fmaak_f32 v50, v19, v48, 0x4b400000
	v_fmaak_f32 v51, v20, v48, 0x4b400000
	v_fmaak_f32 v52, v21, v48, 0x4b400000
	v_perm_b32 v49, v50, v49, s33
	v_perm_b32 v51, v52, v51, s34
	v_or_b32_e32 v56, v49, v51
	v_fmaak_f32 v41, v22, v48, 0x4b400000
	v_fmaak_f32 v42, v23, v48, 0x4b400000
	v_fmaak_f32 v43, v24, v48, 0x4b400000
	v_fmaak_f32 v44, v25, v48, 0x4b400000
	v_perm_b32 v41, v42, v41, s33
	v_perm_b32 v43, v44, v43, s34
	v_or_b32_e32 v57, v41, v43
	v_fmaak_f32 v49, v26, v48, 0x4b400000
	v_fmaak_f32 v50, v27, v48, 0x4b400000
	v_fmaak_f32 v51, v28, v48, 0x4b400000
	v_fmaak_f32 v52, v29, v48, 0x4b400000
	v_perm_b32 v49, v50, v49, s33
	v_perm_b32 v51, v52, v51, s34
	v_or_b32_e32 v58, v49, v51
	v_fmaak_f32 v41, v30, v48, 0x4b400000
	v_fmaak_f32 v42, v31, v48, 0x4b400000
	v_fmaak_f32 v43, v32, v48, 0x4b400000
	v_fmaak_f32 v44, v33, v48, 0x4b400000
	v_perm_b32 v41, v42, v41, s33
	v_perm_b32 v43, v44, v43, s34
	v_or_b32_e32 v59, v41, v43
	s_waitcnt vmcnt(4)
	ds_read_b128 v[18:21], v38 offset:4096
	ds_read_b128 v[22:25], v38 offset:5120
	ds_read_b128 v[26:29], v38 offset:6144
	ds_read_b128 v[30:33], v38 offset:7168
	s_waitcnt lgkmcnt(0)
	s_mov_b32 m0, s36
	s_nop 0
	global_load_lds_dwordx4 v34, s[16:17] nt
	global_load_lds_dwordx4 v34, s[16:17] offset:1024 nt
	global_load_lds_dwordx4 v34, s[16:17] offset:2048 nt
	global_load_lds_dwordx4 v35, s[16:17] offset:3072 nt
	s_add_u32 s16, s16, 0x7d00
	s_addc_u32 s17, s17, 0
	v_cndmask_b32_e64 v30, 0, v30, s[18:19]
	v_cndmask_b32_e64 v31, 0, v31, s[18:19]
	v_cndmask_b32_e64 v32, 0, v32, s[18:19]
	v_cndmask_b32_e64 v33, 0, v33, s[18:19]
	v_max3_f32 v41, |v18|, |v19|, |v20|
	v_max3_f32 v42, |v21|, |v22|, |v23|
	v_max3_f32 v43, |v24|, |v25|, |v26|
	v_max3_f32 v44, |v27|, |v28|, |v29|
	v_max3_f32 v48, |v30|, |v31|, |v32|
	v_max3_f32 v41, v41, v42, |v33|
	v_max3_f32 v43, v43, v44, v48
	v_max_f32_e32 v41, v41, v43
	v_pk_add_f32 v[2:3], v[2:3], v[18:19]
	v_pk_add_f32 v[4:5], v[4:5], v[20:21]
	v_max_f32_dpp v41, v41, v41 quad_perm:[1,0,3,2] row_mask:0xf bank_mask:0xf
	v_pk_add_f32 v[6:7], v[6:7], v[22:23]
	v_pk_add_f32 v[8:9], v[8:9], v[24:25]
	v_max_f32_dpp v41, v41, v41 quad_perm:[2,3,0,1] row_mask:0xf bank_mask:0xf
	v_pk_add_f32 v[10:11], v[10:11], v[26:27]
	v_pk_add_f32 v[12:13], v[12:13], v[28:29]
	v_max_f32_dpp v41, v41, v41 row_half_mirror row_mask:0xf bank_mask:0xf
	v_pk_add_f32 v[14:15], v[14:15], v[30:31]
	v_pk_add_f32 v[16:17], v[16:17], v[32:33]
	v_max_f32_dpp v41, v41, v41 row_mirror row_mask:0xf bank_mask:0xf
	s_nop 1
	v_max_f32_dpp v41, v41, v41 row_bcast:15 row_mask:0xa bank_mask:0xf
	s_nop 1
	v_max_f32_dpp v41, v41, v41 row_bcast:31 row_mask:0xc bank_mask:0xf
	s_nop 1
	v_readlane_b32 s28, v41, 63
	s_nop 1
	v_div_scale_f32 v48, s[30:31], s28, s28, v47
	v_rcp_f32_e32 v49, v48
	s_nop 0
	v_fma_f32 v50, -v48, v49, 1.0
	v_fmac_f32_e32 v49, v50, v49
	v_mov_b32_e32 v50, s28
	v_div_scale_f32 v50, vcc, s32, v50, s32
	v_mul_f32_e32 v51, v50, v49
	v_fma_f32 v52, -v48, v51, v50
	v_fmac_f32_e32 v51, v52, v49
	v_fma_f32 v48, -v48, v51, v50
	v_div_fmas_f32 v48, v48, v49, v51
	v_div_fixup_f32 v48, v48, s28, v47
	v_cmp_gt_f32_e64 vcc, s28, 0
	v_writelane_b32 v40, s28, 1
	s_nop 0
	v_cndmask_b32_e32 v48, 0, v48, vcc
	v_fmaak_f32 v49, v18, v48, 0x4b400000
	v_fmaak_f32 v50, v19, v48, 0x4b400000
	v_fmaak_f32 v51, v20, v48, 0x4b400000
	v_fmaak_f32 v52, v21, v48, 0x4b400000
	v_perm_b32 v49, v50, v49, s33
	v_perm_b32 v51, v52, v51, s34
	v_or_b32_e32 v60, v49, v51
	v_fmaak_f32 v41, v22, v48, 0x4b400000
	v_fmaak_f32 v42, v23, v48, 0x4b400000
	v_fmaak_f32 v43, v24, v48, 0x4b400000
	v_fmaak_f32 v44, v25, v48, 0x4b400000
	v_perm_b32 v41, v42, v41, s33
	v_perm_b32 v43, v44, v43, s34
	v_or_b32_e32 v61, v41, v43
	v_fmaak_f32 v49, v26, v48, 0x4b400000
	v_fmaak_f32 v50, v27, v48, 0x4b400000
	v_fmaak_f32 v51, v28, v48, 0x4b400000
	v_fmaak_f32 v52, v29, v48, 0x4b400000
	v_perm_b32 v49, v50, v49, s33
	v_perm_b32 v51, v52, v51, s34
	v_or_b32_e32 v62, v49, v51
	v_fmaak_f32 v41, v30, v48, 0x4b400000
	v_fmaak_f32 v42, v31, v48, 0x4b400000
	v_fmaak_f32 v43, v32, v48, 0x4b400000
	v_fmaak_f32 v44, v33, v48, 0x4b400000
	v_perm_b32 v41, v42, v41, s33
	v_perm_b32 v43, v44, v43, s34
	v_or_b32_e32 v63, v41, v43
	s_waitcnt vmcnt(4)
	ds_read_b128 v[18:21], v38 offset:0
	ds_read_b128 v[22:25], v38 offset:1024
	ds_read_b128 v[26:29], v38 offset:2048
	ds_read_b128 v[30:33], v38 offset:3072
	s_waitcnt lgkmcnt(0)
	s_mov_b32 m0, s35
	s_nop 0
	global_load_lds_dwordx4 v34, s[16:17] nt
	global_load_lds_dwordx4 v34, s[16:17] offset:1024 nt
	global_load_lds_dwordx4 v34, s[16:17] offset:2048 nt
	global_load_lds_dwordx4 v35, s[16:17] offset:3072 nt
	s_add_u32 s16, s16, 0x7d00
	s_addc_u32 s17, s17, 0
	v_cndmask_b32_e64 v30, 0, v30, s[18:19]
	v_cndmask_b32_e64 v31, 0, v31, s[18:19]
	v_cndmask_b32_e64 v32, 0, v32, s[18:19]
	v_cndmask_b32_e64 v33, 0, v33, s[18:19]
	v_max3_f32 v41, |v18|, |v19|, |v20|
	v_max3_f32 v42, |v21|, |v22|, |v23|
	v_max3_f32 v43, |v24|, |v25|, |v26|
	v_max3_f32 v44, |v27|, |v28|, |v29|
	v_max3_f32 v48, |v30|, |v31|, |v32|
	v_max3_f32 v41, v41, v42, |v33|
	v_max3_f32 v43, v43, v44, v48
	v_max_f32_e32 v41, v41, v43
	v_pk_add_f32 v[2:3], v[2:3], v[18:19]
	v_pk_add_f32 v[4:5], v[4:5], v[20:21]
	v_max_f32_dpp v41, v41, v41 quad_perm:[1,0,3,2] row_mask:0xf bank_mask:0xf
	v_pk_add_f32 v[6:7], v[6:7], v[22:23]
	v_pk_add_f32 v[8:9], v[8:9], v[24:25]
	v_max_f32_dpp v41, v41, v41 quad_perm:[2,3,0,1] row_mask:0xf bank_mask:0xf
	v_pk_add_f32 v[10:11], v[10:11], v[26:27]
	v_pk_add_f32 v[12:13], v[12:13], v[28:29]
	v_max_f32_dpp v41, v41, v41 row_half_mirror row_mask:0xf bank_mask:0xf
	v_pk_add_f32 v[14:15], v[14:15], v[30:31]
	v_pk_add_f32 v[16:17], v[16:17], v[32:33]
	v_max_f32_dpp v41, v41, v41 row_mirror row_mask:0xf bank_mask:0xf
	s_nop 1
	v_max_f32_dpp v41, v41, v41 row_bcast:15 row_mask:0xa bank_mask:0xf
	s_nop 1
	v_max_f32_dpp v41, v41, v41 row_bcast:31 row_mask:0xc bank_mask:0xf
	s_nop 1
	v_readlane_b32 s28, v41, 63
	s_nop 1
	v_div_scale_f32 v48, s[30:31], s28, s28, v47
	v_rcp_f32_e32 v49, v48
	s_nop 0
	v_fma_f32 v50, -v48, v49, 1.0
	v_fmac_f32_e32 v49, v50, v49
	v_mov_b32_e32 v50, s28
	v_div_scale_f32 v50, vcc, s32, v50, s32
	v_mul_f32_e32 v51, v50, v49
	v_fma_f32 v52, -v48, v51, v50
	v_fmac_f32_e32 v51, v52, v49
	v_fma_f32 v48, -v48, v51, v50
	v_div_fmas_f32 v48, v48, v49, v51
	v_div_fixup_f32 v48, v48, s28, v47
	v_cmp_gt_f32_e64 vcc, s28, 0
	v_writelane_b32 v40, s28, 2
	s_nop 0
	v_cndmask_b32_e32 v48, 0, v48, vcc
	v_fmaak_f32 v49, v18, v48, 0x4b400000
	v_fmaak_f32 v50, v19, v48, 0x4b400000
	v_fmaak_f32 v51, v20, v48, 0x4b400000
	v_fmaak_f32 v52, v21, v48, 0x4b400000
	v_perm_b32 v49, v50, v49, s33
	v_perm_b32 v51, v52, v51, s34
	v_or_b32_e32 v64, v49, v51
	v_fmaak_f32 v41, v22, v48, 0x4b400000
	v_fmaak_f32 v42, v23, v48, 0x4b400000
	v_fmaak_f32 v43, v24, v48, 0x4b400000
	v_fmaak_f32 v44, v25, v48, 0x4b400000
	v_perm_b32 v41, v42, v41, s33
	v_perm_b32 v43, v44, v43, s34
	v_or_b32_e32 v65, v41, v43
	v_fmaak_f32 v49, v26, v48, 0x4b400000
	v_fmaak_f32 v50, v27, v48, 0x4b400000
	v_fmaak_f32 v51, v28, v48, 0x4b400000
	v_fmaak_f32 v52, v29, v48, 0x4b400000
	v_perm_b32 v49, v50, v49, s33
	v_perm_b32 v51, v52, v51, s34
	v_or_b32_e32 v66, v49, v51
	v_fmaak_f32 v41, v30, v48, 0x4b400000
	v_fmaak_f32 v42, v31, v48, 0x4b400000
	v_fmaak_f32 v43, v32, v48, 0x4b400000
	v_fmaak_f32 v44, v33, v48, 0x4b400000
	v_perm_b32 v41, v42, v41, s33
	v_perm_b32 v43, v44, v43, s34
	v_or_b32_e32 v67, v41, v43
	s_waitcnt vmcnt(4)
	ds_read_b128 v[18:21], v38 offset:4096
	ds_read_b128 v[22:25], v38 offset:5120
	ds_read_b128 v[26:29], v38 offset:6144
	ds_read_b128 v[30:33], v38 offset:7168
	s_waitcnt lgkmcnt(0)
	s_mov_b32 m0, s36
	s_nop 0
	global_load_lds_dwordx4 v34, s[16:17] nt
	global_load_lds_dwordx4 v34, s[16:17] offset:1024 nt
	global_load_lds_dwordx4 v34, s[16:17] offset:2048 nt
	global_load_lds_dwordx4 v35, s[16:17] offset:3072 nt
	s_add_u32 s16, s16, 0x7d00
	s_addc_u32 s17, s17, 0
	v_cndmask_b32_e64 v30, 0, v30, s[18:19]
	v_cndmask_b32_e64 v31, 0, v31, s[18:19]
	v_cndmask_b32_e64 v32, 0, v32, s[18:19]
	v_cndmask_b32_e64 v33, 0, v33, s[18:19]
	v_max3_f32 v41, |v18|, |v19|, |v20|
	v_max3_f32 v42, |v21|, |v22|, |v23|
	v_max3_f32 v43, |v24|, |v25|, |v26|
	v_max3_f32 v44, |v27|, |v28|, |v29|
	v_max3_f32 v48, |v30|, |v31|, |v32|
	v_max3_f32 v41, v41, v42, |v33|
	v_max3_f32 v43, v43, v44, v48
	v_max_f32_e32 v41, v41, v43
	v_pk_add_f32 v[2:3], v[2:3], v[18:19]
	v_pk_add_f32 v[4:5], v[4:5], v[20:21]
	v_max_f32_dpp v41, v41, v41 quad_perm:[1,0,3,2] row_mask:0xf bank_mask:0xf
	v_pk_add_f32 v[6:7], v[6:7], v[22:23]
	v_pk_add_f32 v[8:9], v[8:9], v[24:25]
	v_max_f32_dpp v41, v41, v41 quad_perm:[2,3,0,1] row_mask:0xf bank_mask:0xf
	v_pk_add_f32 v[10:11], v[10:11], v[26:27]
	v_pk_add_f32 v[12:13], v[12:13], v[28:29]
	v_max_f32_dpp v41, v41, v41 row_half_mirror row_mask:0xf bank_mask:0xf
	v_pk_add_f32 v[14:15], v[14:15], v[30:31]
	v_pk_add_f32 v[16:17], v[16:17], v[32:33]
	v_max_f32_dpp v41, v41, v41 row_mirror row_mask:0xf bank_mask:0xf
	s_nop 1
	v_max_f32_dpp v41, v41, v41 row_bcast:15 row_mask:0xa bank_mask:0xf
	s_nop 1
	v_max_f32_dpp v41, v41, v41 row_bcast:31 row_mask:0xc bank_mask:0xf
	s_nop 1
	v_readlane_b32 s28, v41, 63
	s_nop 1
	v_div_scale_f32 v48, s[30:31], s28, s28, v47
	v_rcp_f32_e32 v49, v48
	s_nop 0
	v_fma_f32 v50, -v48, v49, 1.0
	v_fmac_f32_e32 v49, v50, v49
	v_mov_b32_e32 v50, s28
	v_div_scale_f32 v50, vcc, s32, v50, s32
	v_mul_f32_e32 v51, v50, v49
	v_fma_f32 v52, -v48, v51, v50
	v_fmac_f32_e32 v51, v52, v49
	v_fma_f32 v48, -v48, v51, v50
	v_div_fmas_f32 v48, v48, v49, v51
	v_div_fixup_f32 v48, v48, s28, v47
	v_cmp_gt_f32_e64 vcc, s28, 0
	v_writelane_b32 v40, s28, 3
	s_nop 0
	v_cndmask_b32_e32 v48, 0, v48, vcc
	v_fmaak_f32 v49, v18, v48, 0x4b400000
	v_fmaak_f32 v50, v19, v48, 0x4b400000
	v_fmaak_f32 v51, v20, v48, 0x4b400000
	v_fmaak_f32 v52, v21, v48, 0x4b400000
	v_perm_b32 v49, v50, v49, s33
	v_perm_b32 v51, v52, v51, s34
	v_or_b32_e32 v68, v49, v51
	v_fmaak_f32 v41, v22, v48, 0x4b400000
	v_fmaak_f32 v42, v23, v48, 0x4b400000
	v_fmaak_f32 v43, v24, v48, 0x4b400000
	v_fmaak_f32 v44, v25, v48, 0x4b400000
	v_perm_b32 v41, v42, v41, s33
	v_perm_b32 v43, v44, v43, s34
	v_or_b32_e32 v69, v41, v43
	v_fmaak_f32 v49, v26, v48, 0x4b400000
	v_fmaak_f32 v50, v27, v48, 0x4b400000
	v_fmaak_f32 v51, v28, v48, 0x4b400000
	v_fmaak_f32 v52, v29, v48, 0x4b400000
	v_perm_b32 v49, v50, v49, s33
	v_perm_b32 v51, v52, v51, s34
	v_or_b32_e32 v70, v49, v51
	v_fmaak_f32 v41, v30, v48, 0x4b400000
	v_fmaak_f32 v42, v31, v48, 0x4b400000
	v_fmaak_f32 v43, v32, v48, 0x4b400000
	v_fmaak_f32 v44, v33, v48, 0x4b400000
	v_perm_b32 v41, v42, v41, s33
	v_perm_b32 v43, v44, v43, s34
	v_or_b32_e32 v71, v41, v43
	s_waitcnt vmcnt(4)
	ds_read_b128 v[18:21], v38 offset:0
	ds_read_b128 v[22:25], v38 offset:1024
	ds_read_b128 v[26:29], v38 offset:2048
	ds_read_b128 v[30:33], v38 offset:3072
	s_waitcnt lgkmcnt(0)
	s_mov_b32 m0, s35
	s_nop 0
	global_load_lds_dwordx4 v34, s[16:17] nt
	global_load_lds_dwordx4 v34, s[16:17] offset:1024 nt
	global_load_lds_dwordx4 v34, s[16:17] offset:2048 nt
	global_load_lds_dwordx4 v35, s[16:17] offset:3072 nt
	s_add_u32 s16, s16, 0x7d00
	s_addc_u32 s17, s17, 0
	v_cndmask_b32_e64 v30, 0, v30, s[18:19]
	v_cndmask_b32_e64 v31, 0, v31, s[18:19]
	v_cndmask_b32_e64 v32, 0, v32, s[18:19]
	v_cndmask_b32_e64 v33, 0, v33, s[18:19]
	v_max3_f32 v41, |v18|, |v19|, |v20|
	v_max3_f32 v42, |v21|, |v22|, |v23|
	v_max3_f32 v43, |v24|, |v25|, |v26|
	v_max3_f32 v44, |v27|, |v28|, |v29|
	v_max3_f32 v48, |v30|, |v31|, |v32|
	v_max3_f32 v41, v41, v42, |v33|
	v_max3_f32 v43, v43, v44, v48
	v_max_f32_e32 v41, v41, v43
	v_pk_add_f32 v[2:3], v[2:3], v[18:19]
	v_pk_add_f32 v[4:5], v[4:5], v[20:21]
	v_max_f32_dpp v41, v41, v41 quad_perm:[1,0,3,2] row_mask:0xf bank_mask:0xf
	v_pk_add_f32 v[6:7], v[6:7], v[22:23]
	v_pk_add_f32 v[8:9], v[8:9], v[24:25]
	v_max_f32_dpp v41, v41, v41 quad_perm:[2,3,0,1] row_mask:0xf bank_mask:0xf
	v_pk_add_f32 v[10:11], v[10:11], v[26:27]
	v_pk_add_f32 v[12:13], v[12:13], v[28:29]
	v_max_f32_dpp v41, v41, v41 row_half_mirror row_mask:0xf bank_mask:0xf
	v_pk_add_f32 v[14:15], v[14:15], v[30:31]
	v_pk_add_f32 v[16:17], v[16:17], v[32:33]
	v_max_f32_dpp v41, v41, v41 row_mirror row_mask:0xf bank_mask:0xf
	s_nop 1
	v_max_f32_dpp v41, v41, v41 row_bcast:15 row_mask:0xa bank_mask:0xf
	s_nop 1
	v_max_f32_dpp v41, v41, v41 row_bcast:31 row_mask:0xc bank_mask:0xf
	s_nop 1
	v_readlane_b32 s28, v41, 63
	s_nop 1
	v_div_scale_f32 v48, s[30:31], s28, s28, v47
	v_rcp_f32_e32 v49, v48
	s_nop 0
	v_fma_f32 v50, -v48, v49, 1.0
	v_fmac_f32_e32 v49, v50, v49
	v_mov_b32_e32 v50, s28
	v_div_scale_f32 v50, vcc, s32, v50, s32
	v_mul_f32_e32 v51, v50, v49
	v_fma_f32 v52, -v48, v51, v50
	v_fmac_f32_e32 v51, v52, v49
	v_fma_f32 v48, -v48, v51, v50
	v_div_fmas_f32 v48, v48, v49, v51
	v_div_fixup_f32 v48, v48, s28, v47
	v_cmp_gt_f32_e64 vcc, s28, 0
	v_writelane_b32 v40, s28, 4
	s_nop 0
	v_cndmask_b32_e32 v48, 0, v48, vcc
	v_fmaak_f32 v49, v18, v48, 0x4b400000
	v_fmaak_f32 v50, v19, v48, 0x4b400000
	v_fmaak_f32 v51, v20, v48, 0x4b400000
	v_fmaak_f32 v52, v21, v48, 0x4b400000
	v_perm_b32 v49, v50, v49, s33
	v_perm_b32 v51, v52, v51, s34
	v_or_b32_e32 v72, v49, v51
	v_fmaak_f32 v41, v22, v48, 0x4b400000
	v_fmaak_f32 v42, v23, v48, 0x4b400000
	v_fmaak_f32 v43, v24, v48, 0x4b400000
	v_fmaak_f32 v44, v25, v48, 0x4b400000
	v_perm_b32 v41, v42, v41, s33
	v_perm_b32 v43, v44, v43, s34
	v_or_b32_e32 v73, v41, v43
	v_fmaak_f32 v49, v26, v48, 0x4b400000
	v_fmaak_f32 v50, v27, v48, 0x4b400000
	v_fmaak_f32 v51, v28, v48, 0x4b400000
	v_fmaak_f32 v52, v29, v48, 0x4b400000
	v_perm_b32 v49, v50, v49, s33
	v_perm_b32 v51, v52, v51, s34
	v_or_b32_e32 v74, v49, v51
	v_fmaak_f32 v41, v30, v48, 0x4b400000
	v_fmaak_f32 v42, v31, v48, 0x4b400000
	v_fmaak_f32 v43, v32, v48, 0x4b400000
	v_fmaak_f32 v44, v33, v48, 0x4b400000
	v_perm_b32 v41, v42, v41, s33
	v_perm_b32 v43, v44, v43, s34
	v_or_b32_e32 v75, v41, v43
	s_waitcnt vmcnt(4)
	ds_read_b128 v[18:21], v38 offset:4096
	ds_read_b128 v[22:25], v38 offset:5120
	ds_read_b128 v[26:29], v38 offset:6144
	ds_read_b128 v[30:33], v38 offset:7168
	s_waitcnt lgkmcnt(0)
	s_mov_b32 m0, s36
	s_nop 0
	global_load_lds_dwordx4 v34, s[16:17] nt
	global_load_lds_dwordx4 v34, s[16:17] offset:1024 nt
	global_load_lds_dwordx4 v34, s[16:17] offset:2048 nt
	global_load_lds_dwordx4 v35, s[16:17] offset:3072 nt
	s_add_u32 s16, s16, 0x7d00
	s_addc_u32 s17, s17, 0
	v_cndmask_b32_e64 v30, 0, v30, s[18:19]
	v_cndmask_b32_e64 v31, 0, v31, s[18:19]
	v_cndmask_b32_e64 v32, 0, v32, s[18:19]
	v_cndmask_b32_e64 v33, 0, v33, s[18:19]
	v_max3_f32 v41, |v18|, |v19|, |v20|
	v_max3_f32 v42, |v21|, |v22|, |v23|
	v_max3_f32 v43, |v24|, |v25|, |v26|
	v_max3_f32 v44, |v27|, |v28|, |v29|
	v_max3_f32 v48, |v30|, |v31|, |v32|
	v_max3_f32 v41, v41, v42, |v33|
	v_max3_f32 v43, v43, v44, v48
	v_max_f32_e32 v41, v41, v43
	v_pk_add_f32 v[2:3], v[2:3], v[18:19]
	v_pk_add_f32 v[4:5], v[4:5], v[20:21]
	v_max_f32_dpp v41, v41, v41 quad_perm:[1,0,3,2] row_mask:0xf bank_mask:0xf
	v_pk_add_f32 v[6:7], v[6:7], v[22:23]
	v_pk_add_f32 v[8:9], v[8:9], v[24:25]
	v_max_f32_dpp v41, v41, v41 quad_perm:[2,3,0,1] row_mask:0xf bank_mask:0xf
	v_pk_add_f32 v[10:11], v[10:11], v[26:27]
	v_pk_add_f32 v[12:13], v[12:13], v[28:29]
	v_max_f32_dpp v41, v41, v41 row_half_mirror row_mask:0xf bank_mask:0xf
	v_pk_add_f32 v[14:15], v[14:15], v[30:31]
	v_pk_add_f32 v[16:17], v[16:17], v[32:33]
	v_max_f32_dpp v41, v41, v41 row_mirror row_mask:0xf bank_mask:0xf
	s_nop 1
	v_max_f32_dpp v41, v41, v41 row_bcast:15 row_mask:0xa bank_mask:0xf
	s_nop 1
	v_max_f32_dpp v41, v41, v41 row_bcast:31 row_mask:0xc bank_mask:0xf
	s_nop 1
	v_readlane_b32 s28, v41, 63
	s_nop 1
	v_div_scale_f32 v48, s[30:31], s28, s28, v47
	v_rcp_f32_e32 v49, v48
	s_nop 0
	v_fma_f32 v50, -v48, v49, 1.0
	v_fmac_f32_e32 v49, v50, v49
	v_mov_b32_e32 v50, s28
	v_div_scale_f32 v50, vcc, s32, v50, s32
	v_mul_f32_e32 v51, v50, v49
	v_fma_f32 v52, -v48, v51, v50
	v_fmac_f32_e32 v51, v52, v49
	v_fma_f32 v48, -v48, v51, v50
	v_div_fmas_f32 v48, v48, v49, v51
	v_div_fixup_f32 v48, v48, s28, v47
	v_cmp_gt_f32_e64 vcc, s28, 0
	v_writelane_b32 v40, s28, 5
	s_nop 0
	v_cndmask_b32_e32 v48, 0, v48, vcc
	v_fmaak_f32 v49, v18, v48, 0x4b400000
	v_fmaak_f32 v50, v19, v48, 0x4b400000
	v_fmaak_f32 v51, v20, v48, 0x4b400000
	v_fmaak_f32 v52, v21, v48, 0x4b400000
	v_perm_b32 v49, v50, v49, s33
	v_perm_b32 v51, v52, v51, s34
	v_or_b32_e32 v76, v49, v51
	v_fmaak_f32 v41, v22, v48, 0x4b400000
	v_fmaak_f32 v42, v23, v48, 0x4b400000
	v_fmaak_f32 v43, v24, v48, 0x4b400000
	v_fmaak_f32 v44, v25, v48, 0x4b400000
	v_perm_b32 v41, v42, v41, s33
	v_perm_b32 v43, v44, v43, s34
	v_or_b32_e32 v77, v41, v43
	v_fmaak_f32 v49, v26, v48, 0x4b400000
	v_fmaak_f32 v50, v27, v48, 0x4b400000
	v_fmaak_f32 v51, v28, v48, 0x4b400000
	v_fmaak_f32 v52, v29, v48, 0x4b400000
	v_perm_b32 v49, v50, v49, s33
	v_perm_b32 v51, v52, v51, s34
	v_or_b32_e32 v78, v49, v51
	v_fmaak_f32 v41, v30, v48, 0x4b400000
	v_fmaak_f32 v42, v31, v48, 0x4b400000
	v_fmaak_f32 v43, v32, v48, 0x4b400000
	v_fmaak_f32 v44, v33, v48, 0x4b400000
	v_perm_b32 v41, v42, v41, s33
	v_perm_b32 v43, v44, v43, s34
	v_or_b32_e32 v79, v41, v43
	s_waitcnt vmcnt(4)
	ds_read_b128 v[18:21], v38 offset:0
	ds_read_b128 v[22:25], v38 offset:1024
	ds_read_b128 v[26:29], v38 offset:2048
	ds_read_b128 v[30:33], v38 offset:3072
	s_waitcnt lgkmcnt(0)
	s_mov_b32 m0, s35
	s_nop 0
	global_load_lds_dwordx4 v34, s[16:17] nt
	global_load_lds_dwordx4 v34, s[16:17] offset:1024 nt
	global_load_lds_dwordx4 v34, s[16:17] offset:2048 nt
	global_load_lds_dwordx4 v35, s[16:17] offset:3072 nt
	s_add_u32 s16, s16, 0x7d00
	s_addc_u32 s17, s17, 0
	v_cndmask_b32_e64 v30, 0, v30, s[18:19]
	v_cndmask_b32_e64 v31, 0, v31, s[18:19]
	v_cndmask_b32_e64 v32, 0, v32, s[18:19]
	v_cndmask_b32_e64 v33, 0, v33, s[18:19]
	v_max3_f32 v41, |v18|, |v19|, |v20|
	v_max3_f32 v42, |v21|, |v22|, |v23|
	v_max3_f32 v43, |v24|, |v25|, |v26|
	v_max3_f32 v44, |v27|, |v28|, |v29|
	v_max3_f32 v48, |v30|, |v31|, |v32|
	v_max3_f32 v41, v41, v42, |v33|
	v_max3_f32 v43, v43, v44, v48
	v_max_f32_e32 v41, v41, v43
	v_pk_add_f32 v[2:3], v[2:3], v[18:19]
	v_pk_add_f32 v[4:5], v[4:5], v[20:21]
	v_max_f32_dpp v41, v41, v41 quad_perm:[1,0,3,2] row_mask:0xf bank_mask:0xf
	v_pk_add_f32 v[6:7], v[6:7], v[22:23]
	v_pk_add_f32 v[8:9], v[8:9], v[24:25]
	v_max_f32_dpp v41, v41, v41 quad_perm:[2,3,0,1] row_mask:0xf bank_mask:0xf
	v_pk_add_f32 v[10:11], v[10:11], v[26:27]
	v_pk_add_f32 v[12:13], v[12:13], v[28:29]
	v_max_f32_dpp v41, v41, v41 row_half_mirror row_mask:0xf bank_mask:0xf
	v_pk_add_f32 v[14:15], v[14:15], v[30:31]
	v_pk_add_f32 v[16:17], v[16:17], v[32:33]
	v_max_f32_dpp v41, v41, v41 row_mirror row_mask:0xf bank_mask:0xf
	s_nop 1
	v_max_f32_dpp v41, v41, v41 row_bcast:15 row_mask:0xa bank_mask:0xf
	s_nop 1
	v_max_f32_dpp v41, v41, v41 row_bcast:31 row_mask:0xc bank_mask:0xf
	s_nop 1
	v_readlane_b32 s28, v41, 63
	s_nop 1
	v_div_scale_f32 v48, s[30:31], s28, s28, v47
	v_rcp_f32_e32 v49, v48
	s_nop 0
	v_fma_f32 v50, -v48, v49, 1.0
	v_fmac_f32_e32 v49, v50, v49
	v_mov_b32_e32 v50, s28
	v_div_scale_f32 v50, vcc, s32, v50, s32
	v_mul_f32_e32 v51, v50, v49
	v_fma_f32 v52, -v48, v51, v50
	v_fmac_f32_e32 v51, v52, v49
	v_fma_f32 v48, -v48, v51, v50
	v_div_fmas_f32 v48, v48, v49, v51
	v_div_fixup_f32 v48, v48, s28, v47
	v_cmp_gt_f32_e64 vcc, s28, 0
	v_writelane_b32 v40, s28, 6
	s_nop 0
	v_cndmask_b32_e32 v48, 0, v48, vcc
	v_fmaak_f32 v49, v18, v48, 0x4b400000
	v_fmaak_f32 v50, v19, v48, 0x4b400000
	v_fmaak_f32 v51, v20, v48, 0x4b400000
	v_fmaak_f32 v52, v21, v48, 0x4b400000
	v_perm_b32 v49, v50, v49, s33
	v_perm_b32 v51, v52, v51, s34
	v_or_b32_e32 v80, v49, v51
	v_fmaak_f32 v41, v22, v48, 0x4b400000
	v_fmaak_f32 v42, v23, v48, 0x4b400000
	v_fmaak_f32 v43, v24, v48, 0x4b400000
	v_fmaak_f32 v44, v25, v48, 0x4b400000
	v_perm_b32 v41, v42, v41, s33
	v_perm_b32 v43, v44, v43, s34
	v_or_b32_e32 v81, v41, v43
	v_fmaak_f32 v49, v26, v48, 0x4b400000
	v_fmaak_f32 v50, v27, v48, 0x4b400000
	v_fmaak_f32 v51, v28, v48, 0x4b400000
	v_fmaak_f32 v52, v29, v48, 0x4b400000
	v_perm_b32 v49, v50, v49, s33
	v_perm_b32 v51, v52, v51, s34
	v_or_b32_e32 v82, v49, v51
	v_fmaak_f32 v41, v30, v48, 0x4b400000
	v_fmaak_f32 v42, v31, v48, 0x4b400000
	v_fmaak_f32 v43, v32, v48, 0x4b400000
	v_fmaak_f32 v44, v33, v48, 0x4b400000
	v_perm_b32 v41, v42, v41, s33
	v_perm_b32 v43, v44, v43, s34
	v_or_b32_e32 v83, v41, v43
	s_waitcnt vmcnt(4)
	ds_read_b128 v[18:21], v38 offset:4096
	ds_read_b128 v[22:25], v38 offset:5120
	ds_read_b128 v[26:29], v38 offset:6144
	ds_read_b128 v[30:33], v38 offset:7168
	s_waitcnt lgkmcnt(0)
	s_mov_b32 m0, s36
	s_nop 0
	global_load_lds_dwordx4 v34, s[16:17] nt
	global_load_lds_dwordx4 v34, s[16:17] offset:1024 nt
	global_load_lds_dwordx4 v34, s[16:17] offset:2048 nt
	global_load_lds_dwordx4 v35, s[16:17] offset:3072 nt
	s_add_u32 s16, s16, 0x7d00
	s_addc_u32 s17, s17, 0
	v_cndmask_b32_e64 v30, 0, v30, s[18:19]
	v_cndmask_b32_e64 v31, 0, v31, s[18:19]
	v_cndmask_b32_e64 v32, 0, v32, s[18:19]
	v_cndmask_b32_e64 v33, 0, v33, s[18:19]
	v_max3_f32 v41, |v18|, |v19|, |v20|
	v_max3_f32 v42, |v21|, |v22|, |v23|
	v_max3_f32 v43, |v24|, |v25|, |v26|
	v_max3_f32 v44, |v27|, |v28|, |v29|
	v_max3_f32 v48, |v30|, |v31|, |v32|
	v_max3_f32 v41, v41, v42, |v33|
	v_max3_f32 v43, v43, v44, v48
	v_max_f32_e32 v41, v41, v43
	v_pk_add_f32 v[2:3], v[2:3], v[18:19]
	v_pk_add_f32 v[4:5], v[4:5], v[20:21]
	v_max_f32_dpp v41, v41, v41 quad_perm:[1,0,3,2] row_mask:0xf bank_mask:0xf
	v_pk_add_f32 v[6:7], v[6:7], v[22:23]
	v_pk_add_f32 v[8:9], v[8:9], v[24:25]
	v_max_f32_dpp v41, v41, v41 quad_perm:[2,3,0,1] row_mask:0xf bank_mask:0xf
	v_pk_add_f32 v[10:11], v[10:11], v[26:27]
	v_pk_add_f32 v[12:13], v[12:13], v[28:29]
	v_max_f32_dpp v41, v41, v41 row_half_mirror row_mask:0xf bank_mask:0xf
	v_pk_add_f32 v[14:15], v[14:15], v[30:31]
	v_pk_add_f32 v[16:17], v[16:17], v[32:33]
	v_max_f32_dpp v41, v41, v41 row_mirror row_mask:0xf bank_mask:0xf
	s_nop 1
	v_max_f32_dpp v41, v41, v41 row_bcast:15 row_mask:0xa bank_mask:0xf
	s_nop 1
	v_max_f32_dpp v41, v41, v41 row_bcast:31 row_mask:0xc bank_mask:0xf
	s_nop 1
	v_readlane_b32 s28, v41, 63
	s_nop 1
	v_div_scale_f32 v48, s[30:31], s28, s28, v47
	v_rcp_f32_e32 v49, v48
	s_nop 0
	v_fma_f32 v50, -v48, v49, 1.0
	v_fmac_f32_e32 v49, v50, v49
	v_mov_b32_e32 v50, s28
	v_div_scale_f32 v50, vcc, s32, v50, s32
	v_mul_f32_e32 v51, v50, v49
	v_fma_f32 v52, -v48, v51, v50
	v_fmac_f32_e32 v51, v52, v49
	v_fma_f32 v48, -v48, v51, v50
	v_div_fmas_f32 v48, v48, v49, v51
	v_div_fixup_f32 v48, v48, s28, v47
	v_cmp_gt_f32_e64 vcc, s28, 0
	v_writelane_b32 v40, s28, 7
	s_nop 0
	v_cndmask_b32_e32 v48, 0, v48, vcc
	v_fmaak_f32 v49, v18, v48, 0x4b400000
	v_fmaak_f32 v50, v19, v48, 0x4b400000
	v_fmaak_f32 v51, v20, v48, 0x4b400000
	v_fmaak_f32 v52, v21, v48, 0x4b400000
	v_perm_b32 v49, v50, v49, s33
	v_perm_b32 v51, v52, v51, s34
	v_or_b32_e32 v84, v49, v51
	v_fmaak_f32 v41, v22, v48, 0x4b400000
	v_fmaak_f32 v42, v23, v48, 0x4b400000
	v_fmaak_f32 v43, v24, v48, 0x4b400000
	v_fmaak_f32 v44, v25, v48, 0x4b400000
	v_perm_b32 v41, v42, v41, s33
	v_perm_b32 v43, v44, v43, s34
	v_or_b32_e32 v85, v41, v43
	v_fmaak_f32 v49, v26, v48, 0x4b400000
	v_fmaak_f32 v50, v27, v48, 0x4b400000
	v_fmaak_f32 v51, v28, v48, 0x4b400000
	v_fmaak_f32 v52, v29, v48, 0x4b400000
	v_perm_b32 v49, v50, v49, s33
	v_perm_b32 v51, v52, v51, s34
	v_or_b32_e32 v86, v49, v51
	v_fmaak_f32 v41, v30, v48, 0x4b400000
	v_fmaak_f32 v42, v31, v48, 0x4b400000
	v_fmaak_f32 v43, v32, v48, 0x4b400000
	v_fmaak_f32 v44, v33, v48, 0x4b400000
	v_perm_b32 v41, v42, v41, s33
	v_perm_b32 v43, v44, v43, s34
	v_or_b32_e32 v87, v41, v43
	s_waitcnt vmcnt(4)
	ds_read_b128 v[18:21], v38 offset:0
	ds_read_b128 v[22:25], v38 offset:1024
	ds_read_b128 v[26:29], v38 offset:2048
	ds_read_b128 v[30:33], v38 offset:3072
	s_waitcnt lgkmcnt(0)
	s_mov_b32 m0, s35
	s_nop 0
	global_load_lds_dwordx4 v34, s[16:17] nt
	global_load_lds_dwordx4 v34, s[16:17] offset:1024 nt
	global_load_lds_dwordx4 v34, s[16:17] offset:2048 nt
	global_load_lds_dwordx4 v35, s[16:17] offset:3072 nt
	s_add_u32 s16, s16, 0x7d00
	s_addc_u32 s17, s17, 0
	v_cndmask_b32_e64 v30, 0, v30, s[18:19]
	v_cndmask_b32_e64 v31, 0, v31, s[18:19]
	v_cndmask_b32_e64 v32, 0, v32, s[18:19]
	v_cndmask_b32_e64 v33, 0, v33, s[18:19]
	v_max3_f32 v41, |v18|, |v19|, |v20|
	v_max3_f32 v42, |v21|, |v22|, |v23|
	v_max3_f32 v43, |v24|, |v25|, |v26|
	v_max3_f32 v44, |v27|, |v28|, |v29|
	v_max3_f32 v48, |v30|, |v31|, |v32|
	v_max3_f32 v41, v41, v42, |v33|
	v_max3_f32 v43, v43, v44, v48
	v_max_f32_e32 v41, v41, v43
	v_pk_add_f32 v[2:3], v[2:3], v[18:19]
	v_pk_add_f32 v[4:5], v[4:5], v[20:21]
	v_max_f32_dpp v41, v41, v41 quad_perm:[1,0,3,2] row_mask:0xf bank_mask:0xf
	v_pk_add_f32 v[6:7], v[6:7], v[22:23]
	v_pk_add_f32 v[8:9], v[8:9], v[24:25]
	v_max_f32_dpp v41, v41, v41 quad_perm:[2,3,0,1] row_mask:0xf bank_mask:0xf
	v_pk_add_f32 v[10:11], v[10:11], v[26:27]
	v_pk_add_f32 v[12:13], v[12:13], v[28:29]
	v_max_f32_dpp v41, v41, v41 row_half_mirror row_mask:0xf bank_mask:0xf
	v_pk_add_f32 v[14:15], v[14:15], v[30:31]
	v_pk_add_f32 v[16:17], v[16:17], v[32:33]
	v_max_f32_dpp v41, v41, v41 row_mirror row_mask:0xf bank_mask:0xf
	s_nop 1
	v_max_f32_dpp v41, v41, v41 row_bcast:15 row_mask:0xa bank_mask:0xf
	s_nop 1
	v_max_f32_dpp v41, v41, v41 row_bcast:31 row_mask:0xc bank_mask:0xf
	s_nop 1
	v_readlane_b32 s28, v41, 63
	s_nop 1
	v_div_scale_f32 v48, s[30:31], s28, s28, v47
	v_rcp_f32_e32 v49, v48
	s_nop 0
	v_fma_f32 v50, -v48, v49, 1.0
	v_fmac_f32_e32 v49, v50, v49
	v_mov_b32_e32 v50, s28
	v_div_scale_f32 v50, vcc, s32, v50, s32
	v_mul_f32_e32 v51, v50, v49
	v_fma_f32 v52, -v48, v51, v50
	v_fmac_f32_e32 v51, v52, v49
	v_fma_f32 v48, -v48, v51, v50
	v_div_fmas_f32 v48, v48, v49, v51
	v_div_fixup_f32 v48, v48, s28, v47
	v_cmp_gt_f32_e64 vcc, s28, 0
	v_writelane_b32 v40, s28, 8
	s_nop 0
	v_cndmask_b32_e32 v48, 0, v48, vcc
	v_fmaak_f32 v49, v18, v48, 0x4b400000
	v_fmaak_f32 v50, v19, v48, 0x4b400000
	v_fmaak_f32 v51, v20, v48, 0x4b400000
	v_fmaak_f32 v52, v21, v48, 0x4b400000
	v_perm_b32 v49, v50, v49, s33
	v_perm_b32 v51, v52, v51, s34
	v_or_b32_e32 v88, v49, v51
	v_fmaak_f32 v41, v22, v48, 0x4b400000
	v_fmaak_f32 v42, v23, v48, 0x4b400000
	v_fmaak_f32 v43, v24, v48, 0x4b400000
	v_fmaak_f32 v44, v25, v48, 0x4b400000
	v_perm_b32 v41, v42, v41, s33
	v_perm_b32 v43, v44, v43, s34
	v_or_b32_e32 v89, v41, v43
	v_fmaak_f32 v49, v26, v48, 0x4b400000
	v_fmaak_f32 v50, v27, v48, 0x4b400000
	v_fmaak_f32 v51, v28, v48, 0x4b400000
	v_fmaak_f32 v52, v29, v48, 0x4b400000
	v_perm_b32 v49, v50, v49, s33
	v_perm_b32 v51, v52, v51, s34
	v_or_b32_e32 v90, v49, v51
	v_fmaak_f32 v41, v30, v48, 0x4b400000
	v_fmaak_f32 v42, v31, v48, 0x4b400000
	v_fmaak_f32 v43, v32, v48, 0x4b400000
	v_fmaak_f32 v44, v33, v48, 0x4b400000
	v_perm_b32 v41, v42, v41, s33
	v_perm_b32 v43, v44, v43, s34
	v_or_b32_e32 v91, v41, v43
	s_waitcnt vmcnt(4)
	ds_read_b128 v[18:21], v38 offset:4096
	ds_read_b128 v[22:25], v38 offset:5120
	ds_read_b128 v[26:29], v38 offset:6144
	ds_read_b128 v[30:33], v38 offset:7168
	s_waitcnt lgkmcnt(0)
	s_mov_b32 m0, s36
	s_nop 0
	global_load_lds_dwordx4 v34, s[16:17] nt
	global_load_lds_dwordx4 v34, s[16:17] offset:1024 nt
	global_load_lds_dwordx4 v34, s[16:17] offset:2048 nt
	global_load_lds_dwordx4 v35, s[16:17] offset:3072 nt
	s_add_u32 s16, s16, 0x7d00
	s_addc_u32 s17, s17, 0
	v_cndmask_b32_e64 v30, 0, v30, s[18:19]
	v_cndmask_b32_e64 v31, 0, v31, s[18:19]
	v_cndmask_b32_e64 v32, 0, v32, s[18:19]
	v_cndmask_b32_e64 v33, 0, v33, s[18:19]
	v_max3_f32 v41, |v18|, |v19|, |v20|
	v_max3_f32 v42, |v21|, |v22|, |v23|
	v_max3_f32 v43, |v24|, |v25|, |v26|
	v_max3_f32 v44, |v27|, |v28|, |v29|
	v_max3_f32 v48, |v30|, |v31|, |v32|
	v_max3_f32 v41, v41, v42, |v33|
	v_max3_f32 v43, v43, v44, v48
	v_max_f32_e32 v41, v41, v43
	v_pk_add_f32 v[2:3], v[2:3], v[18:19]
	v_pk_add_f32 v[4:5], v[4:5], v[20:21]
	v_max_f32_dpp v41, v41, v41 quad_perm:[1,0,3,2] row_mask:0xf bank_mask:0xf
	v_pk_add_f32 v[6:7], v[6:7], v[22:23]
	v_pk_add_f32 v[8:9], v[8:9], v[24:25]
	v_max_f32_dpp v41, v41, v41 quad_perm:[2,3,0,1] row_mask:0xf bank_mask:0xf
	v_pk_add_f32 v[10:11], v[10:11], v[26:27]
	v_pk_add_f32 v[12:13], v[12:13], v[28:29]
	v_max_f32_dpp v41, v41, v41 row_half_mirror row_mask:0xf bank_mask:0xf
	v_pk_add_f32 v[14:15], v[14:15], v[30:31]
	v_pk_add_f32 v[16:17], v[16:17], v[32:33]
	v_max_f32_dpp v41, v41, v41 row_mirror row_mask:0xf bank_mask:0xf
	s_nop 1
	v_max_f32_dpp v41, v41, v41 row_bcast:15 row_mask:0xa bank_mask:0xf
	s_nop 1
	v_max_f32_dpp v41, v41, v41 row_bcast:31 row_mask:0xc bank_mask:0xf
	s_nop 1
	v_readlane_b32 s28, v41, 63
	s_nop 1
	v_div_scale_f32 v48, s[30:31], s28, s28, v47
	v_rcp_f32_e32 v49, v48
	s_nop 0
	v_fma_f32 v50, -v48, v49, 1.0
	v_fmac_f32_e32 v49, v50, v49
	v_mov_b32_e32 v50, s28
	v_div_scale_f32 v50, vcc, s32, v50, s32
	v_mul_f32_e32 v51, v50, v49
	v_fma_f32 v52, -v48, v51, v50
	v_fmac_f32_e32 v51, v52, v49
	v_fma_f32 v48, -v48, v51, v50
	v_div_fmas_f32 v48, v48, v49, v51
	v_div_fixup_f32 v48, v48, s28, v47
	v_cmp_gt_f32_e64 vcc, s28, 0
	v_writelane_b32 v40, s28, 9
	s_nop 0
	v_cndmask_b32_e32 v48, 0, v48, vcc
	v_fmaak_f32 v49, v18, v48, 0x4b400000
	v_fmaak_f32 v50, v19, v48, 0x4b400000
	v_fmaak_f32 v51, v20, v48, 0x4b400000
	v_fmaak_f32 v52, v21, v48, 0x4b400000
	v_perm_b32 v49, v50, v49, s33
	v_perm_b32 v51, v52, v51, s34
	v_or_b32_e32 v92, v49, v51
	v_fmaak_f32 v41, v22, v48, 0x4b400000
	v_fmaak_f32 v42, v23, v48, 0x4b400000
	v_fmaak_f32 v43, v24, v48, 0x4b400000
	v_fmaak_f32 v44, v25, v48, 0x4b400000
	v_perm_b32 v41, v42, v41, s33
	v_perm_b32 v43, v44, v43, s34
	v_or_b32_e32 v93, v41, v43
	v_fmaak_f32 v49, v26, v48, 0x4b400000
	v_fmaak_f32 v50, v27, v48, 0x4b400000
	v_fmaak_f32 v51, v28, v48, 0x4b400000
	v_fmaak_f32 v52, v29, v48, 0x4b400000
	v_perm_b32 v49, v50, v49, s33
	v_perm_b32 v51, v52, v51, s34
	v_or_b32_e32 v94, v49, v51
	v_fmaak_f32 v41, v30, v48, 0x4b400000
	v_fmaak_f32 v42, v31, v48, 0x4b400000
	v_fmaak_f32 v43, v32, v48, 0x4b400000
	v_fmaak_f32 v44, v33, v48, 0x4b400000
	v_perm_b32 v41, v42, v41, s33
	v_perm_b32 v43, v44, v43, s34
	v_or_b32_e32 v95, v41, v43
	s_waitcnt vmcnt(4)
	ds_read_b128 v[18:21], v38 offset:0
	ds_read_b128 v[22:25], v38 offset:1024
	ds_read_b128 v[26:29], v38 offset:2048
	ds_read_b128 v[30:33], v38 offset:3072
	s_waitcnt lgkmcnt(0)
	s_mov_b32 m0, s35
	s_nop 0
	global_load_lds_dwordx4 v34, s[16:17] nt
	global_load_lds_dwordx4 v34, s[16:17] offset:1024 nt
	global_load_lds_dwordx4 v34, s[16:17] offset:2048 nt
	global_load_lds_dwordx4 v35, s[16:17] offset:3072 nt
	s_add_u32 s16, s16, 0x7d00
	s_addc_u32 s17, s17, 0
	v_cndmask_b32_e64 v30, 0, v30, s[18:19]
	v_cndmask_b32_e64 v31, 0, v31, s[18:19]
	v_cndmask_b32_e64 v32, 0, v32, s[18:19]
	v_cndmask_b32_e64 v33, 0, v33, s[18:19]
	v_max3_f32 v41, |v18|, |v19|, |v20|
	v_max3_f32 v42, |v21|, |v22|, |v23|
	v_max3_f32 v43, |v24|, |v25|, |v26|
	v_max3_f32 v44, |v27|, |v28|, |v29|
	v_max3_f32 v48, |v30|, |v31|, |v32|
	v_max3_f32 v41, v41, v42, |v33|
	v_max3_f32 v43, v43, v44, v48
	v_max_f32_e32 v41, v41, v43
	v_pk_add_f32 v[2:3], v[2:3], v[18:19]
	v_pk_add_f32 v[4:5], v[4:5], v[20:21]
	v_max_f32_dpp v41, v41, v41 quad_perm:[1,0,3,2] row_mask:0xf bank_mask:0xf
	v_pk_add_f32 v[6:7], v[6:7], v[22:23]
	v_pk_add_f32 v[8:9], v[8:9], v[24:25]
	v_max_f32_dpp v41, v41, v41 quad_perm:[2,3,0,1] row_mask:0xf bank_mask:0xf
	v_pk_add_f32 v[10:11], v[10:11], v[26:27]
	v_pk_add_f32 v[12:13], v[12:13], v[28:29]
	v_max_f32_dpp v41, v41, v41 row_half_mirror row_mask:0xf bank_mask:0xf
	v_pk_add_f32 v[14:15], v[14:15], v[30:31]
	v_pk_add_f32 v[16:17], v[16:17], v[32:33]
	v_max_f32_dpp v41, v41, v41 row_mirror row_mask:0xf bank_mask:0xf
	s_nop 1
	v_max_f32_dpp v41, v41, v41 row_bcast:15 row_mask:0xa bank_mask:0xf
	s_nop 1
	v_max_f32_dpp v41, v41, v41 row_bcast:31 row_mask:0xc bank_mask:0xf
	s_nop 1
	v_readlane_b32 s28, v41, 63
	s_nop 1
	v_div_scale_f32 v48, s[30:31], s28, s28, v47
	v_rcp_f32_e32 v49, v48
	s_nop 0
	v_fma_f32 v50, -v48, v49, 1.0
	v_fmac_f32_e32 v49, v50, v49
	v_mov_b32_e32 v50, s28
	v_div_scale_f32 v50, vcc, s32, v50, s32
	v_mul_f32_e32 v51, v50, v49
	v_fma_f32 v52, -v48, v51, v50
	v_fmac_f32_e32 v51, v52, v49
	v_fma_f32 v48, -v48, v51, v50
	v_div_fmas_f32 v48, v48, v49, v51
	v_div_fixup_f32 v48, v48, s28, v47
	v_cmp_gt_f32_e64 vcc, s28, 0
	v_writelane_b32 v40, s28, 10
	s_nop 0
	v_cndmask_b32_e32 v48, 0, v48, vcc
	v_fmaak_f32 v49, v18, v48, 0x4b400000
	v_fmaak_f32 v50, v19, v48, 0x4b400000
	v_fmaak_f32 v51, v20, v48, 0x4b400000
	v_fmaak_f32 v52, v21, v48, 0x4b400000
	v_perm_b32 v49, v50, v49, s33
	v_perm_b32 v51, v52, v51, s34
	v_or_b32_e32 v96, v49, v51
	v_fmaak_f32 v41, v22, v48, 0x4b400000
	v_fmaak_f32 v42, v23, v48, 0x4b400000
	v_fmaak_f32 v43, v24, v48, 0x4b400000
	v_fmaak_f32 v44, v25, v48, 0x4b400000
	v_perm_b32 v41, v42, v41, s33
	v_perm_b32 v43, v44, v43, s34
	v_or_b32_e32 v97, v41, v43
	v_fmaak_f32 v49, v26, v48, 0x4b400000
	v_fmaak_f32 v50, v27, v48, 0x4b400000
	v_fmaak_f32 v51, v28, v48, 0x4b400000
	v_fmaak_f32 v52, v29, v48, 0x4b400000
	v_perm_b32 v49, v50, v49, s33
	v_perm_b32 v51, v52, v51, s34
	v_or_b32_e32 v98, v49, v51
	v_fmaak_f32 v41, v30, v48, 0x4b400000
	v_fmaak_f32 v42, v31, v48, 0x4b400000
	v_fmaak_f32 v43, v32, v48, 0x4b400000
	v_fmaak_f32 v44, v33, v48, 0x4b400000
	v_perm_b32 v41, v42, v41, s33
	v_perm_b32 v43, v44, v43, s34
	v_or_b32_e32 v99, v41, v43
	s_waitcnt vmcnt(4)
	ds_read_b128 v[18:21], v38 offset:4096
	ds_read_b128 v[22:25], v38 offset:5120
	ds_read_b128 v[26:29], v38 offset:6144
	ds_read_b128 v[30:33], v38 offset:7168
	s_waitcnt lgkmcnt(0)
	s_mov_b32 m0, s36
	s_nop 0
	global_load_lds_dwordx4 v34, s[16:17] nt
	global_load_lds_dwordx4 v34, s[16:17] offset:1024 nt
	global_load_lds_dwordx4 v34, s[16:17] offset:2048 nt
	global_load_lds_dwordx4 v35, s[16:17] offset:3072 nt
	s_add_u32 s16, s16, 0x7d00
	s_addc_u32 s17, s17, 0
	v_cndmask_b32_e64 v30, 0, v30, s[18:19]
	v_cndmask_b32_e64 v31, 0, v31, s[18:19]
	v_cndmask_b32_e64 v32, 0, v32, s[18:19]
	v_cndmask_b32_e64 v33, 0, v33, s[18:19]
	v_max3_f32 v41, |v18|, |v19|, |v20|
	v_max3_f32 v42, |v21|, |v22|, |v23|
	v_max3_f32 v43, |v24|, |v25|, |v26|
	v_max3_f32 v44, |v27|, |v28|, |v29|
	v_max3_f32 v48, |v30|, |v31|, |v32|
	v_max3_f32 v41, v41, v42, |v33|
	v_max3_f32 v43, v43, v44, v48
	v_max_f32_e32 v41, v41, v43
	v_pk_add_f32 v[2:3], v[2:3], v[18:19]
	v_pk_add_f32 v[4:5], v[4:5], v[20:21]
	v_max_f32_dpp v41, v41, v41 quad_perm:[1,0,3,2] row_mask:0xf bank_mask:0xf
	v_pk_add_f32 v[6:7], v[6:7], v[22:23]
	v_pk_add_f32 v[8:9], v[8:9], v[24:25]
	v_max_f32_dpp v41, v41, v41 quad_perm:[2,3,0,1] row_mask:0xf bank_mask:0xf
	v_pk_add_f32 v[10:11], v[10:11], v[26:27]
	v_pk_add_f32 v[12:13], v[12:13], v[28:29]
	v_max_f32_dpp v41, v41, v41 row_half_mirror row_mask:0xf bank_mask:0xf
	v_pk_add_f32 v[14:15], v[14:15], v[30:31]
	v_pk_add_f32 v[16:17], v[16:17], v[32:33]
	v_max_f32_dpp v41, v41, v41 row_mirror row_mask:0xf bank_mask:0xf
	s_nop 1
	v_max_f32_dpp v41, v41, v41 row_bcast:15 row_mask:0xa bank_mask:0xf
	s_nop 1
	v_max_f32_dpp v41, v41, v41 row_bcast:31 row_mask:0xc bank_mask:0xf
	s_nop 1
	v_readlane_b32 s28, v41, 63
	s_nop 1
	v_div_scale_f32 v48, s[30:31], s28, s28, v47
	v_rcp_f32_e32 v49, v48
	s_nop 0
	v_fma_f32 v50, -v48, v49, 1.0
	v_fmac_f32_e32 v49, v50, v49
	v_mov_b32_e32 v50, s28
	v_div_scale_f32 v50, vcc, s32, v50, s32
	v_mul_f32_e32 v51, v50, v49
	v_fma_f32 v52, -v48, v51, v50
	v_fmac_f32_e32 v51, v52, v49
	v_fma_f32 v48, -v48, v51, v50
	v_div_fmas_f32 v48, v48, v49, v51
	v_div_fixup_f32 v48, v48, s28, v47
	v_cmp_gt_f32_e64 vcc, s28, 0
	v_writelane_b32 v40, s28, 11
	s_nop 0
	v_cndmask_b32_e32 v48, 0, v48, vcc
	v_fmaak_f32 v49, v18, v48, 0x4b400000
	v_fmaak_f32 v50, v19, v48, 0x4b400000
	v_fmaak_f32 v51, v20, v48, 0x4b400000
	v_fmaak_f32 v52, v21, v48, 0x4b400000
	v_perm_b32 v49, v50, v49, s33
	v_perm_b32 v51, v52, v51, s34
	v_or_b32_e32 v100, v49, v51
	v_fmaak_f32 v41, v22, v48, 0x4b400000
	v_fmaak_f32 v42, v23, v48, 0x4b400000
	v_fmaak_f32 v43, v24, v48, 0x4b400000
	v_fmaak_f32 v44, v25, v48, 0x4b400000
	v_perm_b32 v41, v42, v41, s33
	v_perm_b32 v43, v44, v43, s34
	v_or_b32_e32 v101, v41, v43
	v_fmaak_f32 v49, v26, v48, 0x4b400000
	v_fmaak_f32 v50, v27, v48, 0x4b400000
	v_fmaak_f32 v51, v28, v48, 0x4b400000
	v_fmaak_f32 v52, v29, v48, 0x4b400000
	v_perm_b32 v49, v50, v49, s33
	v_perm_b32 v51, v52, v51, s34
	v_or_b32_e32 v102, v49, v51
	v_fmaak_f32 v41, v30, v48, 0x4b400000
	v_fmaak_f32 v42, v31, v48, 0x4b400000
	v_fmaak_f32 v43, v32, v48, 0x4b400000
	v_fmaak_f32 v44, v33, v48, 0x4b400000
	v_perm_b32 v41, v42, v41, s33
	v_perm_b32 v43, v44, v43, s34
	v_or_b32_e32 v103, v41, v43
	s_waitcnt vmcnt(4)
	ds_read_b128 v[18:21], v38 offset:0
	ds_read_b128 v[22:25], v38 offset:1024
	ds_read_b128 v[26:29], v38 offset:2048
	ds_read_b128 v[30:33], v38 offset:3072
	s_waitcnt lgkmcnt(0)
	s_mov_b32 m0, s35
	s_nop 0
	global_load_lds_dwordx4 v34, s[16:17] nt
	global_load_lds_dwordx4 v34, s[16:17] offset:1024 nt
	global_load_lds_dwordx4 v34, s[16:17] offset:2048 nt
	global_load_lds_dwordx4 v35, s[16:17] offset:3072 nt
	s_add_u32 s16, s16, 0x7d00
	s_addc_u32 s17, s17, 0
	v_cndmask_b32_e64 v30, 0, v30, s[18:19]
	v_cndmask_b32_e64 v31, 0, v31, s[18:19]
	v_cndmask_b32_e64 v32, 0, v32, s[18:19]
	v_cndmask_b32_e64 v33, 0, v33, s[18:19]
	v_max3_f32 v41, |v18|, |v19|, |v20|
	v_max3_f32 v42, |v21|, |v22|, |v23|
	v_max3_f32 v43, |v24|, |v25|, |v26|
	v_max3_f32 v44, |v27|, |v28|, |v29|
	v_max3_f32 v48, |v30|, |v31|, |v32|
	v_max3_f32 v41, v41, v42, |v33|
	v_max3_f32 v43, v43, v44, v48
	v_max_f32_e32 v41, v41, v43
	v_pk_add_f32 v[2:3], v[2:3], v[18:19]
	v_pk_add_f32 v[4:5], v[4:5], v[20:21]
	v_max_f32_dpp v41, v41, v41 quad_perm:[1,0,3,2] row_mask:0xf bank_mask:0xf
	v_pk_add_f32 v[6:7], v[6:7], v[22:23]
	v_pk_add_f32 v[8:9], v[8:9], v[24:25]
	v_max_f32_dpp v41, v41, v41 quad_perm:[2,3,0,1] row_mask:0xf bank_mask:0xf
	v_pk_add_f32 v[10:11], v[10:11], v[26:27]
	v_pk_add_f32 v[12:13], v[12:13], v[28:29]
	v_max_f32_dpp v41, v41, v41 row_half_mirror row_mask:0xf bank_mask:0xf
	v_pk_add_f32 v[14:15], v[14:15], v[30:31]
	v_pk_add_f32 v[16:17], v[16:17], v[32:33]
	v_max_f32_dpp v41, v41, v41 row_mirror row_mask:0xf bank_mask:0xf
	s_nop 1
	v_max_f32_dpp v41, v41, v41 row_bcast:15 row_mask:0xa bank_mask:0xf
	s_nop 1
	v_max_f32_dpp v41, v41, v41 row_bcast:31 row_mask:0xc bank_mask:0xf
	s_nop 1
	v_readlane_b32 s28, v41, 63
	s_nop 1
	v_div_scale_f32 v48, s[30:31], s28, s28, v47
	v_rcp_f32_e32 v49, v48
	s_nop 0
	v_fma_f32 v50, -v48, v49, 1.0
	v_fmac_f32_e32 v49, v50, v49
	v_mov_b32_e32 v50, s28
	v_div_scale_f32 v50, vcc, s32, v50, s32
	v_mul_f32_e32 v51, v50, v49
	v_fma_f32 v52, -v48, v51, v50
	v_fmac_f32_e32 v51, v52, v49
	v_fma_f32 v48, -v48, v51, v50
	v_div_fmas_f32 v48, v48, v49, v51
	v_div_fixup_f32 v48, v48, s28, v47
	v_cmp_gt_f32_e64 vcc, s28, 0
	v_writelane_b32 v40, s28, 12
	s_nop 0
	v_cndmask_b32_e32 v48, 0, v48, vcc
	v_fmaak_f32 v49, v18, v48, 0x4b400000
	v_fmaak_f32 v50, v19, v48, 0x4b400000
	v_fmaak_f32 v51, v20, v48, 0x4b400000
	v_fmaak_f32 v52, v21, v48, 0x4b400000
	v_perm_b32 v49, v50, v49, s33
	v_perm_b32 v51, v52, v51, s34
	v_or_b32_e32 v104, v49, v51
	v_fmaak_f32 v41, v22, v48, 0x4b400000
	v_fmaak_f32 v42, v23, v48, 0x4b400000
	v_fmaak_f32 v43, v24, v48, 0x4b400000
	v_fmaak_f32 v44, v25, v48, 0x4b400000
	v_perm_b32 v41, v42, v41, s33
	v_perm_b32 v43, v44, v43, s34
	v_or_b32_e32 v105, v41, v43
	v_fmaak_f32 v49, v26, v48, 0x4b400000
	v_fmaak_f32 v50, v27, v48, 0x4b400000
	v_fmaak_f32 v51, v28, v48, 0x4b400000
	v_fmaak_f32 v52, v29, v48, 0x4b400000
	v_perm_b32 v49, v50, v49, s33
	v_perm_b32 v51, v52, v51, s34
	v_or_b32_e32 v106, v49, v51
	v_fmaak_f32 v41, v30, v48, 0x4b400000
	v_fmaak_f32 v42, v31, v48, 0x4b400000
	v_fmaak_f32 v43, v32, v48, 0x4b400000
	v_fmaak_f32 v44, v33, v48, 0x4b400000
	v_perm_b32 v41, v42, v41, s33
	v_perm_b32 v43, v44, v43, s34
	v_or_b32_e32 v107, v41, v43
	s_waitcnt vmcnt(4)
	ds_read_b128 v[18:21], v38 offset:4096
	ds_read_b128 v[22:25], v38 offset:5120
	ds_read_b128 v[26:29], v38 offset:6144
	ds_read_b128 v[30:33], v38 offset:7168
	s_waitcnt lgkmcnt(0)
	s_mov_b32 m0, s36
	s_nop 0
	global_load_lds_dwordx4 v34, s[16:17] nt
	global_load_lds_dwordx4 v34, s[16:17] offset:1024 nt
	global_load_lds_dwordx4 v34, s[16:17] offset:2048 nt
	global_load_lds_dwordx4 v35, s[16:17] offset:3072 nt
	s_add_u32 s16, s16, 0x7d00
	s_addc_u32 s17, s17, 0
	v_cndmask_b32_e64 v30, 0, v30, s[18:19]
	v_cndmask_b32_e64 v31, 0, v31, s[18:19]
	v_cndmask_b32_e64 v32, 0, v32, s[18:19]
	v_cndmask_b32_e64 v33, 0, v33, s[18:19]
	v_max3_f32 v41, |v18|, |v19|, |v20|
	v_max3_f32 v42, |v21|, |v22|, |v23|
	v_max3_f32 v43, |v24|, |v25|, |v26|
	v_max3_f32 v44, |v27|, |v28|, |v29|
	v_max3_f32 v48, |v30|, |v31|, |v32|
	v_max3_f32 v41, v41, v42, |v33|
	v_max3_f32 v43, v43, v44, v48
	v_max_f32_e32 v41, v41, v43
	v_pk_add_f32 v[2:3], v[2:3], v[18:19]
	v_pk_add_f32 v[4:5], v[4:5], v[20:21]
	v_max_f32_dpp v41, v41, v41 quad_perm:[1,0,3,2] row_mask:0xf bank_mask:0xf
	v_pk_add_f32 v[6:7], v[6:7], v[22:23]
	v_pk_add_f32 v[8:9], v[8:9], v[24:25]
	v_max_f32_dpp v41, v41, v41 quad_perm:[2,3,0,1] row_mask:0xf bank_mask:0xf
	v_pk_add_f32 v[10:11], v[10:11], v[26:27]
	v_pk_add_f32 v[12:13], v[12:13], v[28:29]
	v_max_f32_dpp v41, v41, v41 row_half_mirror row_mask:0xf bank_mask:0xf
	v_pk_add_f32 v[14:15], v[14:15], v[30:31]
	v_pk_add_f32 v[16:17], v[16:17], v[32:33]
	v_max_f32_dpp v41, v41, v41 row_mirror row_mask:0xf bank_mask:0xf
	s_nop 1
	v_max_f32_dpp v41, v41, v41 row_bcast:15 row_mask:0xa bank_mask:0xf
	s_nop 1
	v_max_f32_dpp v41, v41, v41 row_bcast:31 row_mask:0xc bank_mask:0xf
	s_nop 1
	v_readlane_b32 s28, v41, 63
	s_nop 1
	v_div_scale_f32 v48, s[30:31], s28, s28, v47
	v_rcp_f32_e32 v49, v48
	s_nop 0
	v_fma_f32 v50, -v48, v49, 1.0
	v_fmac_f32_e32 v49, v50, v49
	v_mov_b32_e32 v50, s28
	v_div_scale_f32 v50, vcc, s32, v50, s32
	v_mul_f32_e32 v51, v50, v49
	v_fma_f32 v52, -v48, v51, v50
	v_fmac_f32_e32 v51, v52, v49
	v_fma_f32 v48, -v48, v51, v50
	v_div_fmas_f32 v48, v48, v49, v51
	v_div_fixup_f32 v48, v48, s28, v47
	v_cmp_gt_f32_e64 vcc, s28, 0
	v_writelane_b32 v40, s28, 13
	s_nop 0
	v_cndmask_b32_e32 v48, 0, v48, vcc
	v_fmaak_f32 v49, v18, v48, 0x4b400000
	v_fmaak_f32 v50, v19, v48, 0x4b400000
	v_fmaak_f32 v51, v20, v48, 0x4b400000
	v_fmaak_f32 v52, v21, v48, 0x4b400000
	v_perm_b32 v49, v50, v49, s33
	v_perm_b32 v51, v52, v51, s34
	v_or_b32_e32 v108, v49, v51
	v_fmaak_f32 v41, v22, v48, 0x4b400000
	v_fmaak_f32 v42, v23, v48, 0x4b400000
	v_fmaak_f32 v43, v24, v48, 0x4b400000
	v_fmaak_f32 v44, v25, v48, 0x4b400000
	v_perm_b32 v41, v42, v41, s33
	v_perm_b32 v43, v44, v43, s34
	v_or_b32_e32 v109, v41, v43
	v_fmaak_f32 v49, v26, v48, 0x4b400000
	v_fmaak_f32 v50, v27, v48, 0x4b400000
	v_fmaak_f32 v51, v28, v48, 0x4b400000
	v_fmaak_f32 v52, v29, v48, 0x4b400000
	v_perm_b32 v49, v50, v49, s33
	v_perm_b32 v51, v52, v51, s34
	v_or_b32_e32 v110, v49, v51
	v_fmaak_f32 v41, v30, v48, 0x4b400000
	v_fmaak_f32 v42, v31, v48, 0x4b400000
	v_fmaak_f32 v43, v32, v48, 0x4b400000
	v_fmaak_f32 v44, v33, v48, 0x4b400000
	v_perm_b32 v41, v42, v41, s33
	v_perm_b32 v43, v44, v43, s34
	v_or_b32_e32 v111, v41, v43
	s_waitcnt vmcnt(4)
	ds_read_b128 v[18:21], v38 offset:0
	ds_read_b128 v[22:25], v38 offset:1024
	ds_read_b128 v[26:29], v38 offset:2048
	ds_read_b128 v[30:33], v38 offset:3072
	s_waitcnt lgkmcnt(0)
	s_mov_b32 m0, s35
	s_nop 0
	global_load_lds_dwordx4 v34, s[16:17] nt
	global_load_lds_dwordx4 v34, s[16:17] offset:1024 nt
	global_load_lds_dwordx4 v34, s[16:17] offset:2048 nt
	global_load_lds_dwordx4 v35, s[16:17] offset:3072 nt
	s_add_u32 s16, s16, 0x7d00
	s_addc_u32 s17, s17, 0
	v_cndmask_b32_e64 v30, 0, v30, s[18:19]
	v_cndmask_b32_e64 v31, 0, v31, s[18:19]
	v_cndmask_b32_e64 v32, 0, v32, s[18:19]
	v_cndmask_b32_e64 v33, 0, v33, s[18:19]
	v_max3_f32 v41, |v18|, |v19|, |v20|
	v_max3_f32 v42, |v21|, |v22|, |v23|
	v_max3_f32 v43, |v24|, |v25|, |v26|
	v_max3_f32 v44, |v27|, |v28|, |v29|
	v_max3_f32 v48, |v30|, |v31|, |v32|
	v_max3_f32 v41, v41, v42, |v33|
	v_max3_f32 v43, v43, v44, v48
	v_max_f32_e32 v41, v41, v43
	v_pk_add_f32 v[2:3], v[2:3], v[18:19]
	v_pk_add_f32 v[4:5], v[4:5], v[20:21]
	v_max_f32_dpp v41, v41, v41 quad_perm:[1,0,3,2] row_mask:0xf bank_mask:0xf
	v_pk_add_f32 v[6:7], v[6:7], v[22:23]
	v_pk_add_f32 v[8:9], v[8:9], v[24:25]
	v_max_f32_dpp v41, v41, v41 quad_perm:[2,3,0,1] row_mask:0xf bank_mask:0xf
	v_pk_add_f32 v[10:11], v[10:11], v[26:27]
	v_pk_add_f32 v[12:13], v[12:13], v[28:29]
	v_max_f32_dpp v41, v41, v41 row_half_mirror row_mask:0xf bank_mask:0xf
	v_pk_add_f32 v[14:15], v[14:15], v[30:31]
	v_pk_add_f32 v[16:17], v[16:17], v[32:33]
	v_max_f32_dpp v41, v41, v41 row_mirror row_mask:0xf bank_mask:0xf
	s_nop 1
	v_max_f32_dpp v41, v41, v41 row_bcast:15 row_mask:0xa bank_mask:0xf
	s_nop 1
	v_max_f32_dpp v41, v41, v41 row_bcast:31 row_mask:0xc bank_mask:0xf
	s_nop 1
	v_readlane_b32 s28, v41, 63
	s_nop 1
	v_div_scale_f32 v48, s[30:31], s28, s28, v47
	v_rcp_f32_e32 v49, v48
	s_nop 0
	v_fma_f32 v50, -v48, v49, 1.0
	v_fmac_f32_e32 v49, v50, v49
	v_mov_b32_e32 v50, s28
	v_div_scale_f32 v50, vcc, s32, v50, s32
	v_mul_f32_e32 v51, v50, v49
	v_fma_f32 v52, -v48, v51, v50
	v_fmac_f32_e32 v51, v52, v49
	v_fma_f32 v48, -v48, v51, v50
	v_div_fmas_f32 v48, v48, v49, v51
	v_div_fixup_f32 v48, v48, s28, v47
	v_cmp_gt_f32_e64 vcc, s28, 0
	v_writelane_b32 v40, s28, 14
	s_nop 0
	v_cndmask_b32_e32 v48, 0, v48, vcc
	v_fmaak_f32 v49, v18, v48, 0x4b400000
	v_fmaak_f32 v50, v19, v48, 0x4b400000
	v_fmaak_f32 v51, v20, v48, 0x4b400000
	v_fmaak_f32 v52, v21, v48, 0x4b400000
	v_perm_b32 v49, v50, v49, s33
	v_perm_b32 v51, v52, v51, s34
	v_or_b32_e32 v112, v49, v51
	v_fmaak_f32 v41, v22, v48, 0x4b400000
	v_fmaak_f32 v42, v23, v48, 0x4b400000
	v_fmaak_f32 v43, v24, v48, 0x4b400000
	v_fmaak_f32 v44, v25, v48, 0x4b400000
	v_perm_b32 v41, v42, v41, s33
	v_perm_b32 v43, v44, v43, s34
	v_or_b32_e32 v113, v41, v43
	v_fmaak_f32 v49, v26, v48, 0x4b400000
	v_fmaak_f32 v50, v27, v48, 0x4b400000
	v_fmaak_f32 v51, v28, v48, 0x4b400000
	v_fmaak_f32 v52, v29, v48, 0x4b400000
	v_perm_b32 v49, v50, v49, s33
	v_perm_b32 v51, v52, v51, s34
	v_or_b32_e32 v114, v49, v51
	v_fmaak_f32 v41, v30, v48, 0x4b400000
	v_fmaak_f32 v42, v31, v48, 0x4b400000
	v_fmaak_f32 v43, v32, v48, 0x4b400000
	v_fmaak_f32 v44, v33, v48, 0x4b400000
	v_perm_b32 v41, v42, v41, s33
	v_perm_b32 v43, v44, v43, s34
	v_or_b32_e32 v115, v41, v43
	s_waitcnt vmcnt(4)
	ds_read_b128 v[18:21], v38 offset:4096
	ds_read_b128 v[22:25], v38 offset:5120
	ds_read_b128 v[26:29], v38 offset:6144
	ds_read_b128 v[30:33], v38 offset:7168
	s_waitcnt lgkmcnt(0)
	s_mov_b32 m0, s36
	s_nop 0
	global_load_lds_dwordx4 v34, s[16:17] nt
	global_load_lds_dwordx4 v34, s[16:17] offset:1024 nt
	global_load_lds_dwordx4 v34, s[16:17] offset:2048 nt
	global_load_lds_dwordx4 v35, s[16:17] offset:3072 nt
	s_add_u32 s16, s16, 0x7d00
	s_addc_u32 s17, s17, 0
	v_cndmask_b32_e64 v30, 0, v30, s[18:19]
	v_cndmask_b32_e64 v31, 0, v31, s[18:19]
	v_cndmask_b32_e64 v32, 0, v32, s[18:19]
	v_cndmask_b32_e64 v33, 0, v33, s[18:19]
	v_max3_f32 v41, |v18|, |v19|, |v20|
	v_max3_f32 v42, |v21|, |v22|, |v23|
	v_max3_f32 v43, |v24|, |v25|, |v26|
	v_max3_f32 v44, |v27|, |v28|, |v29|
	v_max3_f32 v48, |v30|, |v31|, |v32|
	v_max3_f32 v41, v41, v42, |v33|
	v_max3_f32 v43, v43, v44, v48
	v_max_f32_e32 v41, v41, v43
	v_pk_add_f32 v[2:3], v[2:3], v[18:19]
	v_pk_add_f32 v[4:5], v[4:5], v[20:21]
	v_max_f32_dpp v41, v41, v41 quad_perm:[1,0,3,2] row_mask:0xf bank_mask:0xf
	v_pk_add_f32 v[6:7], v[6:7], v[22:23]
	v_pk_add_f32 v[8:9], v[8:9], v[24:25]
	v_max_f32_dpp v41, v41, v41 quad_perm:[2,3,0,1] row_mask:0xf bank_mask:0xf
	v_pk_add_f32 v[10:11], v[10:11], v[26:27]
	v_pk_add_f32 v[12:13], v[12:13], v[28:29]
	v_max_f32_dpp v41, v41, v41 row_half_mirror row_mask:0xf bank_mask:0xf
	v_pk_add_f32 v[14:15], v[14:15], v[30:31]
	v_pk_add_f32 v[16:17], v[16:17], v[32:33]
	v_max_f32_dpp v41, v41, v41 row_mirror row_mask:0xf bank_mask:0xf
	s_nop 1
	v_max_f32_dpp v41, v41, v41 row_bcast:15 row_mask:0xa bank_mask:0xf
	s_nop 1
	v_max_f32_dpp v41, v41, v41 row_bcast:31 row_mask:0xc bank_mask:0xf
	s_nop 1
	v_readlane_b32 s28, v41, 63
	s_nop 1
	v_div_scale_f32 v48, s[30:31], s28, s28, v47
	v_rcp_f32_e32 v49, v48
	s_nop 0
	v_fma_f32 v50, -v48, v49, 1.0
	v_fmac_f32_e32 v49, v50, v49
	v_mov_b32_e32 v50, s28
	v_div_scale_f32 v50, vcc, s32, v50, s32
	v_mul_f32_e32 v51, v50, v49
	v_fma_f32 v52, -v48, v51, v50
	v_fmac_f32_e32 v51, v52, v49
	v_fma_f32 v48, -v48, v51, v50
	v_div_fmas_f32 v48, v48, v49, v51
	v_div_fixup_f32 v48, v48, s28, v47
	v_cmp_gt_f32_e64 vcc, s28, 0
	v_writelane_b32 v40, s28, 15
	s_nop 0
	v_cndmask_b32_e32 v48, 0, v48, vcc
	v_fmaak_f32 v49, v18, v48, 0x4b400000
	v_fmaak_f32 v50, v19, v48, 0x4b400000
	v_fmaak_f32 v51, v20, v48, 0x4b400000
	v_fmaak_f32 v52, v21, v48, 0x4b400000
	v_perm_b32 v49, v50, v49, s33
	v_perm_b32 v51, v52, v51, s34
	v_or_b32_e32 v116, v49, v51
	v_fmaak_f32 v41, v22, v48, 0x4b400000
	v_fmaak_f32 v42, v23, v48, 0x4b400000
	v_fmaak_f32 v43, v24, v48, 0x4b400000
	v_fmaak_f32 v44, v25, v48, 0x4b400000
	v_perm_b32 v41, v42, v41, s33
	v_perm_b32 v43, v44, v43, s34
	v_or_b32_e32 v117, v41, v43
	v_fmaak_f32 v49, v26, v48, 0x4b400000
	v_fmaak_f32 v50, v27, v48, 0x4b400000
	v_fmaak_f32 v51, v28, v48, 0x4b400000
	v_fmaak_f32 v52, v29, v48, 0x4b400000
	v_perm_b32 v49, v50, v49, s33
	v_perm_b32 v51, v52, v51, s34
	v_or_b32_e32 v118, v49, v51
	v_fmaak_f32 v41, v30, v48, 0x4b400000
	v_fmaak_f32 v42, v31, v48, 0x4b400000
	v_fmaak_f32 v43, v32, v48, 0x4b400000
	v_fmaak_f32 v44, v33, v48, 0x4b400000
	v_perm_b32 v41, v42, v41, s33
	v_perm_b32 v43, v44, v43, s34
	v_or_b32_e32 v119, v41, v43
	s_waitcnt vmcnt(4)
	ds_read_b128 v[18:21], v38 offset:0
	ds_read_b128 v[22:25], v38 offset:1024
	ds_read_b128 v[26:29], v38 offset:2048
	ds_read_b128 v[30:33], v38 offset:3072
	s_waitcnt lgkmcnt(0)
	s_mov_b32 m0, s35
	s_nop 0
	global_load_lds_dwordx4 v34, s[16:17] nt
	global_load_lds_dwordx4 v34, s[16:17] offset:1024 nt
	global_load_lds_dwordx4 v34, s[16:17] offset:2048 nt
	global_load_lds_dwordx4 v35, s[16:17] offset:3072 nt
	s_add_u32 s16, s16, 0x7d00
	s_addc_u32 s17, s17, 0
	v_cndmask_b32_e64 v30, 0, v30, s[18:19]
	v_cndmask_b32_e64 v31, 0, v31, s[18:19]
	v_cndmask_b32_e64 v32, 0, v32, s[18:19]
	v_cndmask_b32_e64 v33, 0, v33, s[18:19]
	v_max3_f32 v41, |v18|, |v19|, |v20|
	v_max3_f32 v42, |v21|, |v22|, |v23|
	v_max3_f32 v43, |v24|, |v25|, |v26|
	v_max3_f32 v44, |v27|, |v28|, |v29|
	v_max3_f32 v48, |v30|, |v31|, |v32|
	v_max3_f32 v41, v41, v42, |v33|
	v_max3_f32 v43, v43, v44, v48
	v_max_f32_e32 v41, v41, v43
	v_pk_add_f32 v[2:3], v[2:3], v[18:19]
	v_pk_add_f32 v[4:5], v[4:5], v[20:21]
	v_max_f32_dpp v41, v41, v41 quad_perm:[1,0,3,2] row_mask:0xf bank_mask:0xf
	v_pk_add_f32 v[6:7], v[6:7], v[22:23]
	v_pk_add_f32 v[8:9], v[8:9], v[24:25]
	v_max_f32_dpp v41, v41, v41 quad_perm:[2,3,0,1] row_mask:0xf bank_mask:0xf
	v_pk_add_f32 v[10:11], v[10:11], v[26:27]
	v_pk_add_f32 v[12:13], v[12:13], v[28:29]
	v_max_f32_dpp v41, v41, v41 row_half_mirror row_mask:0xf bank_mask:0xf
	v_pk_add_f32 v[14:15], v[14:15], v[30:31]
	v_pk_add_f32 v[16:17], v[16:17], v[32:33]
	v_max_f32_dpp v41, v41, v41 row_mirror row_mask:0xf bank_mask:0xf
	s_nop 1
	v_max_f32_dpp v41, v41, v41 row_bcast:15 row_mask:0xa bank_mask:0xf
	s_nop 1
	v_max_f32_dpp v41, v41, v41 row_bcast:31 row_mask:0xc bank_mask:0xf
	s_nop 1
	v_readlane_b32 s28, v41, 63
	s_nop 1
	v_div_scale_f32 v48, s[30:31], s28, s28, v47
	v_rcp_f32_e32 v49, v48
	s_nop 0
	v_fma_f32 v50, -v48, v49, 1.0
	v_fmac_f32_e32 v49, v50, v49
	v_mov_b32_e32 v50, s28
	v_div_scale_f32 v50, vcc, s32, v50, s32
	v_mul_f32_e32 v51, v50, v49
	v_fma_f32 v52, -v48, v51, v50
	v_fmac_f32_e32 v51, v52, v49
	v_fma_f32 v48, -v48, v51, v50
	v_div_fmas_f32 v48, v48, v49, v51
	v_div_fixup_f32 v48, v48, s28, v47
	v_cmp_gt_f32_e64 vcc, s28, 0
	v_writelane_b32 v40, s28, 16
	s_nop 0
	v_cndmask_b32_e32 v48, 0, v48, vcc
	v_fmaak_f32 v49, v18, v48, 0x4b400000
	v_fmaak_f32 v50, v19, v48, 0x4b400000
	v_fmaak_f32 v51, v20, v48, 0x4b400000
	v_fmaak_f32 v52, v21, v48, 0x4b400000
	v_perm_b32 v49, v50, v49, s33
	v_perm_b32 v51, v52, v51, s34
	v_or_b32_e32 v120, v49, v51
	v_fmaak_f32 v41, v22, v48, 0x4b400000
	v_fmaak_f32 v42, v23, v48, 0x4b400000
	v_fmaak_f32 v43, v24, v48, 0x4b400000
	v_fmaak_f32 v44, v25, v48, 0x4b400000
	v_perm_b32 v41, v42, v41, s33
	v_perm_b32 v43, v44, v43, s34
	v_or_b32_e32 v121, v41, v43
	v_fmaak_f32 v49, v26, v48, 0x4b400000
	v_fmaak_f32 v50, v27, v48, 0x4b400000
	v_fmaak_f32 v51, v28, v48, 0x4b400000
	v_fmaak_f32 v52, v29, v48, 0x4b400000
	v_perm_b32 v49, v50, v49, s33
	v_perm_b32 v51, v52, v51, s34
	v_or_b32_e32 v122, v49, v51
	v_fmaak_f32 v41, v30, v48, 0x4b400000
	v_fmaak_f32 v42, v31, v48, 0x4b400000
	v_fmaak_f32 v43, v32, v48, 0x4b400000
	v_fmaak_f32 v44, v33, v48, 0x4b400000
	v_perm_b32 v41, v42, v41, s33
	v_perm_b32 v43, v44, v43, s34
	v_or_b32_e32 v123, v41, v43
	s_waitcnt vmcnt(4)
	ds_read_b128 v[18:21], v38 offset:4096
	ds_read_b128 v[22:25], v38 offset:5120
	ds_read_b128 v[26:29], v38 offset:6144
	ds_read_b128 v[30:33], v38 offset:7168
	s_waitcnt lgkmcnt(0)
	s_mov_b32 m0, s36
	s_nop 0
	global_load_lds_dwordx4 v34, s[16:17] nt
	global_load_lds_dwordx4 v34, s[16:17] offset:1024 nt
	global_load_lds_dwordx4 v34, s[16:17] offset:2048 nt
	global_load_lds_dwordx4 v35, s[16:17] offset:3072 nt
	s_add_u32 s16, s16, 0x7d00
	s_addc_u32 s17, s17, 0
	v_cndmask_b32_e64 v30, 0, v30, s[18:19]
	v_cndmask_b32_e64 v31, 0, v31, s[18:19]
	v_cndmask_b32_e64 v32, 0, v32, s[18:19]
	v_cndmask_b32_e64 v33, 0, v33, s[18:19]
	v_max3_f32 v41, |v18|, |v19|, |v20|
	v_max3_f32 v42, |v21|, |v22|, |v23|
	v_max3_f32 v43, |v24|, |v25|, |v26|
	v_max3_f32 v44, |v27|, |v28|, |v29|
	v_max3_f32 v48, |v30|, |v31|, |v32|
	v_max3_f32 v41, v41, v42, |v33|
	v_max3_f32 v43, v43, v44, v48
	v_max_f32_e32 v41, v41, v43
	v_pk_add_f32 v[2:3], v[2:3], v[18:19]
	v_pk_add_f32 v[4:5], v[4:5], v[20:21]
	v_max_f32_dpp v41, v41, v41 quad_perm:[1,0,3,2] row_mask:0xf bank_mask:0xf
	v_pk_add_f32 v[6:7], v[6:7], v[22:23]
	v_pk_add_f32 v[8:9], v[8:9], v[24:25]
	v_max_f32_dpp v41, v41, v41 quad_perm:[2,3,0,1] row_mask:0xf bank_mask:0xf
	v_pk_add_f32 v[10:11], v[10:11], v[26:27]
	v_pk_add_f32 v[12:13], v[12:13], v[28:29]
	v_max_f32_dpp v41, v41, v41 row_half_mirror row_mask:0xf bank_mask:0xf
	v_pk_add_f32 v[14:15], v[14:15], v[30:31]
	v_pk_add_f32 v[16:17], v[16:17], v[32:33]
	v_max_f32_dpp v41, v41, v41 row_mirror row_mask:0xf bank_mask:0xf
	s_nop 1
	v_max_f32_dpp v41, v41, v41 row_bcast:15 row_mask:0xa bank_mask:0xf
	s_nop 1
	v_max_f32_dpp v41, v41, v41 row_bcast:31 row_mask:0xc bank_mask:0xf
	s_nop 1
	v_readlane_b32 s28, v41, 63
	s_nop 1
	v_div_scale_f32 v48, s[30:31], s28, s28, v47
	v_rcp_f32_e32 v49, v48
	s_nop 0
	v_fma_f32 v50, -v48, v49, 1.0
	v_fmac_f32_e32 v49, v50, v49
	v_mov_b32_e32 v50, s28
	v_div_scale_f32 v50, vcc, s32, v50, s32
	v_mul_f32_e32 v51, v50, v49
	v_fma_f32 v52, -v48, v51, v50
	v_fmac_f32_e32 v51, v52, v49
	v_fma_f32 v48, -v48, v51, v50
	v_div_fmas_f32 v48, v48, v49, v51
	v_div_fixup_f32 v48, v48, s28, v47
	v_cmp_gt_f32_e64 vcc, s28, 0
	v_writelane_b32 v40, s28, 17
	s_nop 0
	v_cndmask_b32_e32 v48, 0, v48, vcc
	v_fmaak_f32 v49, v18, v48, 0x4b400000
	v_fmaak_f32 v50, v19, v48, 0x4b400000
	v_fmaak_f32 v51, v20, v48, 0x4b400000
	v_fmaak_f32 v52, v21, v48, 0x4b400000
	v_perm_b32 v49, v50, v49, s33
	v_perm_b32 v51, v52, v51, s34
	v_or_b32_e32 v124, v49, v51
	v_fmaak_f32 v41, v22, v48, 0x4b400000
	v_fmaak_f32 v42, v23, v48, 0x4b400000
	v_fmaak_f32 v43, v24, v48, 0x4b400000
	v_fmaak_f32 v44, v25, v48, 0x4b400000
	v_perm_b32 v41, v42, v41, s33
	v_perm_b32 v43, v44, v43, s34
	v_or_b32_e32 v125, v41, v43
	v_fmaak_f32 v49, v26, v48, 0x4b400000
	v_fmaak_f32 v50, v27, v48, 0x4b400000
	v_fmaak_f32 v51, v28, v48, 0x4b400000
	v_fmaak_f32 v52, v29, v48, 0x4b400000
	v_perm_b32 v49, v50, v49, s33
	v_perm_b32 v51, v52, v51, s34
	v_or_b32_e32 v126, v49, v51
	v_fmaak_f32 v41, v30, v48, 0x4b400000
	v_fmaak_f32 v42, v31, v48, 0x4b400000
	v_fmaak_f32 v43, v32, v48, 0x4b400000
	v_fmaak_f32 v44, v33, v48, 0x4b400000
	v_perm_b32 v41, v42, v41, s33
	v_perm_b32 v43, v44, v43, s34
	v_or_b32_e32 v127, v41, v43
	s_waitcnt vmcnt(4)
	ds_read_b128 v[18:21], v38 offset:0
	ds_read_b128 v[22:25], v38 offset:1024
	ds_read_b128 v[26:29], v38 offset:2048
	ds_read_b128 v[30:33], v38 offset:3072
	s_waitcnt lgkmcnt(0)
	s_mov_b32 m0, s35
	s_nop 0
	global_load_lds_dwordx4 v34, s[16:17] nt
	global_load_lds_dwordx4 v34, s[16:17] offset:1024 nt
	global_load_lds_dwordx4 v34, s[16:17] offset:2048 nt
	global_load_lds_dwordx4 v35, s[16:17] offset:3072 nt
	s_add_u32 s16, s16, 0x7d00
	s_addc_u32 s17, s17, 0
	v_cndmask_b32_e64 v30, 0, v30, s[18:19]
	v_cndmask_b32_e64 v31, 0, v31, s[18:19]
	v_cndmask_b32_e64 v32, 0, v32, s[18:19]
	v_cndmask_b32_e64 v33, 0, v33, s[18:19]
	v_max3_f32 v41, |v18|, |v19|, |v20|
	v_max3_f32 v42, |v21|, |v22|, |v23|
	v_max3_f32 v43, |v24|, |v25|, |v26|
	v_max3_f32 v44, |v27|, |v28|, |v29|
	v_max3_f32 v48, |v30|, |v31|, |v32|
	v_max3_f32 v41, v41, v42, |v33|
	v_max3_f32 v43, v43, v44, v48
	v_max_f32_e32 v41, v41, v43
	v_pk_add_f32 v[2:3], v[2:3], v[18:19]
	v_pk_add_f32 v[4:5], v[4:5], v[20:21]
	v_max_f32_dpp v41, v41, v41 quad_perm:[1,0,3,2] row_mask:0xf bank_mask:0xf
	v_pk_add_f32 v[6:7], v[6:7], v[22:23]
	v_pk_add_f32 v[8:9], v[8:9], v[24:25]
	v_max_f32_dpp v41, v41, v41 quad_perm:[2,3,0,1] row_mask:0xf bank_mask:0xf
	v_pk_add_f32 v[10:11], v[10:11], v[26:27]
	v_pk_add_f32 v[12:13], v[12:13], v[28:29]
	v_max_f32_dpp v41, v41, v41 row_half_mirror row_mask:0xf bank_mask:0xf
	v_pk_add_f32 v[14:15], v[14:15], v[30:31]
	v_pk_add_f32 v[16:17], v[16:17], v[32:33]
	v_max_f32_dpp v41, v41, v41 row_mirror row_mask:0xf bank_mask:0xf
	s_nop 1
	v_max_f32_dpp v41, v41, v41 row_bcast:15 row_mask:0xa bank_mask:0xf
	s_nop 1
	v_max_f32_dpp v41, v41, v41 row_bcast:31 row_mask:0xc bank_mask:0xf
	s_nop 1
	v_readlane_b32 s28, v41, 63
	s_nop 1
	v_div_scale_f32 v48, s[30:31], s28, s28, v47
	v_rcp_f32_e32 v49, v48
	s_nop 0
	v_fma_f32 v50, -v48, v49, 1.0
	v_fmac_f32_e32 v49, v50, v49
	v_mov_b32_e32 v50, s28
	v_div_scale_f32 v50, vcc, s32, v50, s32
	v_mul_f32_e32 v51, v50, v49
	v_fma_f32 v52, -v48, v51, v50
	v_fmac_f32_e32 v51, v52, v49
	v_fma_f32 v48, -v48, v51, v50
	v_div_fmas_f32 v48, v48, v49, v51
	v_div_fixup_f32 v48, v48, s28, v47
	v_cmp_gt_f32_e64 vcc, s28, 0
	v_writelane_b32 v40, s28, 18
	s_nop 0
	v_cndmask_b32_e32 v48, 0, v48, vcc
	v_fmaak_f32 v49, v18, v48, 0x4b400000
	v_fmaak_f32 v50, v19, v48, 0x4b400000
	v_fmaak_f32 v51, v20, v48, 0x4b400000
	v_fmaak_f32 v52, v21, v48, 0x4b400000
	v_perm_b32 v49, v50, v49, s33
	v_perm_b32 v51, v52, v51, s34
	v_or_b32_e32 v49, v49, v51
	s_add_u32 s20, s20, 0x4800
	s_addc_u32 s21, s21, 0
	s_add_u32 s22, s22, 0x4800
	s_addc_u32 s23, s23, 0
	s_add_u32 s24, s24, 0x4800
	s_addc_u32 s25, s25, 0
	s_add_u32 s26, s26, 0x4800
	s_addc_u32 s27, s27, 0
	global_store_dword v39, v49, s[20:21]
	v_fmaak_f32 v41, v22, v48, 0x4b400000
	v_fmaak_f32 v42, v23, v48, 0x4b400000
	v_fmaak_f32 v43, v24, v48, 0x4b400000
	v_fmaak_f32 v44, v25, v48, 0x4b400000
	v_perm_b32 v41, v42, v41, s33
	v_perm_b32 v43, v44, v43, s34
	v_or_b32_e32 v41, v41, v43
	global_store_dword v39, v41, s[22:23]
	v_fmaak_f32 v49, v26, v48, 0x4b400000
	v_fmaak_f32 v50, v27, v48, 0x4b400000
	v_fmaak_f32 v51, v28, v48, 0x4b400000
	v_fmaak_f32 v52, v29, v48, 0x4b400000
	v_perm_b32 v49, v50, v49, s33
	v_perm_b32 v51, v52, v51, s34
	v_or_b32_e32 v49, v49, v51
	global_store_dword v39, v49, s[24:25]
	v_fmaak_f32 v41, v30, v48, 0x4b400000
	v_fmaak_f32 v42, v31, v48, 0x4b400000
	v_fmaak_f32 v43, v32, v48, 0x4b400000
	v_fmaak_f32 v44, v33, v48, 0x4b400000
	v_perm_b32 v41, v42, v41, s33
	v_perm_b32 v43, v44, v43, s34
	v_or_b32_e32 v41, v41, v43
	global_store_dword v39, v41, s[26:27]
	s_waitcnt vmcnt(8)
	ds_read_b128 v[18:21], v38 offset:4096
	ds_read_b128 v[22:25], v38 offset:5120
	ds_read_b128 v[26:29], v38 offset:6144
	ds_read_b128 v[30:33], v38 offset:7168
	s_waitcnt lgkmcnt(0)
	s_mov_b32 m0, s36
	s_nop 0
	global_load_lds_dwordx4 v34, s[16:17] nt
	global_load_lds_dwordx4 v34, s[16:17] offset:1024 nt
	global_load_lds_dwordx4 v34, s[16:17] offset:2048 nt
	global_load_lds_dwordx4 v35, s[16:17] offset:3072 nt
	s_add_u32 s16, s16, 0x7d00
	s_addc_u32 s17, s17, 0
	v_cndmask_b32_e64 v30, 0, v30, s[18:19]
	v_cndmask_b32_e64 v31, 0, v31, s[18:19]
	v_cndmask_b32_e64 v32, 0, v32, s[18:19]
	v_cndmask_b32_e64 v33, 0, v33, s[18:19]
	v_max3_f32 v41, |v18|, |v19|, |v20|
	v_max3_f32 v42, |v21|, |v22|, |v23|
	v_max3_f32 v43, |v24|, |v25|, |v26|
	v_max3_f32 v44, |v27|, |v28|, |v29|
	v_max3_f32 v48, |v30|, |v31|, |v32|
	v_max3_f32 v41, v41, v42, |v33|
	v_max3_f32 v43, v43, v44, v48
	v_max_f32_e32 v41, v41, v43
	v_pk_add_f32 v[2:3], v[2:3], v[18:19]
	v_pk_add_f32 v[4:5], v[4:5], v[20:21]
	v_max_f32_dpp v41, v41, v41 quad_perm:[1,0,3,2] row_mask:0xf bank_mask:0xf
	v_pk_add_f32 v[6:7], v[6:7], v[22:23]
	v_pk_add_f32 v[8:9], v[8:9], v[24:25]
	v_max_f32_dpp v41, v41, v41 quad_perm:[2,3,0,1] row_mask:0xf bank_mask:0xf
	v_pk_add_f32 v[10:11], v[10:11], v[26:27]
	v_pk_add_f32 v[12:13], v[12:13], v[28:29]
	v_max_f32_dpp v41, v41, v41 row_half_mirror row_mask:0xf bank_mask:0xf
	v_pk_add_f32 v[14:15], v[14:15], v[30:31]
	v_pk_add_f32 v[16:17], v[16:17], v[32:33]
	v_max_f32_dpp v41, v41, v41 row_mirror row_mask:0xf bank_mask:0xf
	s_nop 1
	v_max_f32_dpp v41, v41, v41 row_bcast:15 row_mask:0xa bank_mask:0xf
	s_nop 1
	v_max_f32_dpp v41, v41, v41 row_bcast:31 row_mask:0xc bank_mask:0xf
	s_nop 1
	v_readlane_b32 s28, v41, 63
	s_nop 1
	v_div_scale_f32 v48, s[30:31], s28, s28, v47
	v_rcp_f32_e32 v49, v48
	s_nop 0
	v_fma_f32 v50, -v48, v49, 1.0
	v_fmac_f32_e32 v49, v50, v49
	v_mov_b32_e32 v50, s28
	v_div_scale_f32 v50, vcc, s32, v50, s32
	v_mul_f32_e32 v51, v50, v49
	v_fma_f32 v52, -v48, v51, v50
	v_fmac_f32_e32 v51, v52, v49
	v_fma_f32 v48, -v48, v51, v50
	v_div_fmas_f32 v48, v48, v49, v51
	v_div_fixup_f32 v48, v48, s28, v47
	v_cmp_gt_f32_e64 vcc, s28, 0
	v_writelane_b32 v40, s28, 19
	s_nop 0
	v_cndmask_b32_e32 v48, 0, v48, vcc
	v_fmaak_f32 v49, v18, v48, 0x4b400000
	v_fmaak_f32 v50, v19, v48, 0x4b400000
	v_fmaak_f32 v51, v20, v48, 0x4b400000
	v_fmaak_f32 v52, v21, v48, 0x4b400000
	v_perm_b32 v49, v50, v49, s33
	v_perm_b32 v51, v52, v51, s34
	v_or_b32_e32 v49, v49, v51
	s_add_u32 s20, s20, 0x400
	s_addc_u32 s21, s21, 0
	s_add_u32 s22, s22, 0x400
	s_addc_u32 s23, s23, 0
	s_add_u32 s24, s24, 0x400
	s_addc_u32 s25, s25, 0
	s_add_u32 s26, s26, 0x400
	s_addc_u32 s27, s27, 0
	global_store_dword v39, v49, s[20:21]
	v_fmaak_f32 v41, v22, v48, 0x4b400000
	v_fmaak_f32 v42, v23, v48, 0x4b400000
	v_fmaak_f32 v43, v24, v48, 0x4b400000
	v_fmaak_f32 v44, v25, v48, 0x4b400000
	v_perm_b32 v41, v42, v41, s33
	v_perm_b32 v43, v44, v43, s34
	v_or_b32_e32 v41, v41, v43
	global_store_dword v39, v41, s[22:23]
	v_fmaak_f32 v49, v26, v48, 0x4b400000
	v_fmaak_f32 v50, v27, v48, 0x4b400000
	v_fmaak_f32 v51, v28, v48, 0x4b400000
	v_fmaak_f32 v52, v29, v48, 0x4b400000
	v_perm_b32 v49, v50, v49, s33
	v_perm_b32 v51, v52, v51, s34
	v_or_b32_e32 v49, v49, v51
	global_store_dword v39, v49, s[24:25]
	v_fmaak_f32 v41, v30, v48, 0x4b400000
	v_fmaak_f32 v42, v31, v48, 0x4b400000
	v_fmaak_f32 v43, v32, v48, 0x4b400000
	v_fmaak_f32 v44, v33, v48, 0x4b400000
	v_perm_b32 v41, v42, v41, s33
	v_perm_b32 v43, v44, v43, s34
	v_or_b32_e32 v41, v41, v43
	global_store_dword v39, v41, s[26:27]
	s_waitcnt vmcnt(12)
	ds_read_b128 v[18:21], v38 offset:0
	ds_read_b128 v[22:25], v38 offset:1024
	ds_read_b128 v[26:29], v38 offset:2048
	ds_read_b128 v[30:33], v38 offset:3072
	s_waitcnt lgkmcnt(0)
	s_mov_b32 m0, s35
	s_nop 0
	global_load_lds_dwordx4 v34, s[16:17] nt
	global_load_lds_dwordx4 v34, s[16:17] offset:1024 nt
	global_load_lds_dwordx4 v34, s[16:17] offset:2048 nt
	global_load_lds_dwordx4 v35, s[16:17] offset:3072 nt
	s_add_u32 s16, s16, 0x7d00
	s_addc_u32 s17, s17, 0
	v_cndmask_b32_e64 v30, 0, v30, s[18:19]
	v_cndmask_b32_e64 v31, 0, v31, s[18:19]
	v_cndmask_b32_e64 v32, 0, v32, s[18:19]
	v_cndmask_b32_e64 v33, 0, v33, s[18:19]
	v_max3_f32 v41, |v18|, |v19|, |v20|
	v_max3_f32 v42, |v21|, |v22|, |v23|
	v_max3_f32 v43, |v24|, |v25|, |v26|
	v_max3_f32 v44, |v27|, |v28|, |v29|
	v_max3_f32 v48, |v30|, |v31|, |v32|
	v_max3_f32 v41, v41, v42, |v33|
	v_max3_f32 v43, v43, v44, v48
	v_max_f32_e32 v41, v41, v43
	v_pk_add_f32 v[2:3], v[2:3], v[18:19]
	v_pk_add_f32 v[4:5], v[4:5], v[20:21]
	v_max_f32_dpp v41, v41, v41 quad_perm:[1,0,3,2] row_mask:0xf bank_mask:0xf
	v_pk_add_f32 v[6:7], v[6:7], v[22:23]
	v_pk_add_f32 v[8:9], v[8:9], v[24:25]
	v_max_f32_dpp v41, v41, v41 quad_perm:[2,3,0,1] row_mask:0xf bank_mask:0xf
	v_pk_add_f32 v[10:11], v[10:11], v[26:27]
	v_pk_add_f32 v[12:13], v[12:13], v[28:29]
	v_max_f32_dpp v41, v41, v41 row_half_mirror row_mask:0xf bank_mask:0xf
	v_pk_add_f32 v[14:15], v[14:15], v[30:31]
	v_pk_add_f32 v[16:17], v[16:17], v[32:33]
	v_max_f32_dpp v41, v41, v41 row_mirror row_mask:0xf bank_mask:0xf
	s_nop 1
	v_max_f32_dpp v41, v41, v41 row_bcast:15 row_mask:0xa bank_mask:0xf
	s_nop 1
	v_max_f32_dpp v41, v41, v41 row_bcast:31 row_mask:0xc bank_mask:0xf
	s_nop 1
	v_readlane_b32 s28, v41, 63
	s_nop 1
	v_div_scale_f32 v48, s[30:31], s28, s28, v47
	v_rcp_f32_e32 v49, v48
	s_nop 0
	v_fma_f32 v50, -v48, v49, 1.0
	v_fmac_f32_e32 v49, v50, v49
	v_mov_b32_e32 v50, s28
	v_div_scale_f32 v50, vcc, s32, v50, s32
	v_mul_f32_e32 v51, v50, v49
	v_fma_f32 v52, -v48, v51, v50
	v_fmac_f32_e32 v51, v52, v49
	v_fma_f32 v48, -v48, v51, v50
	v_div_fmas_f32 v48, v48, v49, v51
	v_div_fixup_f32 v48, v48, s28, v47
	v_cmp_gt_f32_e64 vcc, s28, 0
	v_writelane_b32 v40, s28, 20
	s_nop 0
	v_cndmask_b32_e32 v48, 0, v48, vcc
	v_fmaak_f32 v49, v18, v48, 0x4b400000
	v_fmaak_f32 v50, v19, v48, 0x4b400000
	v_fmaak_f32 v51, v20, v48, 0x4b400000
	v_fmaak_f32 v52, v21, v48, 0x4b400000
	v_perm_b32 v49, v50, v49, s33
	v_perm_b32 v51, v52, v51, s34
	v_or_b32_e32 v49, v49, v51
	s_add_u32 s20, s20, 0x400
	s_addc_u32 s21, s21, 0
	s_add_u32 s22, s22, 0x400
	s_addc_u32 s23, s23, 0
	s_add_u32 s24, s24, 0x400
	s_addc_u32 s25, s25, 0
	s_add_u32 s26, s26, 0x400
	s_addc_u32 s27, s27, 0
	global_store_dword v39, v49, s[20:21]
	v_fmaak_f32 v41, v22, v48, 0x4b400000
	v_fmaak_f32 v42, v23, v48, 0x4b400000
	v_fmaak_f32 v43, v24, v48, 0x4b400000
	v_fmaak_f32 v44, v25, v48, 0x4b400000
	v_perm_b32 v41, v42, v41, s33
	v_perm_b32 v43, v44, v43, s34
	v_or_b32_e32 v41, v41, v43
	global_store_dword v39, v41, s[22:23]
	v_fmaak_f32 v49, v26, v48, 0x4b400000
	v_fmaak_f32 v50, v27, v48, 0x4b400000
	v_fmaak_f32 v51, v28, v48, 0x4b400000
	v_fmaak_f32 v52, v29, v48, 0x4b400000
	v_perm_b32 v49, v50, v49, s33
	v_perm_b32 v51, v52, v51, s34
	v_or_b32_e32 v49, v49, v51
	global_store_dword v39, v49, s[24:25]
	v_fmaak_f32 v41, v30, v48, 0x4b400000
	v_fmaak_f32 v42, v31, v48, 0x4b400000
	v_fmaak_f32 v43, v32, v48, 0x4b400000
	v_fmaak_f32 v44, v33, v48, 0x4b400000
	v_perm_b32 v41, v42, v41, s33
	v_perm_b32 v43, v44, v43, s34
	v_or_b32_e32 v41, v41, v43
	global_store_dword v39, v41, s[26:27]
	s_waitcnt vmcnt(12)
	ds_read_b128 v[18:21], v38 offset:4096
	ds_read_b128 v[22:25], v38 offset:5120
	ds_read_b128 v[26:29], v38 offset:6144
	ds_read_b128 v[30:33], v38 offset:7168
	s_waitcnt lgkmcnt(0)
	s_mov_b32 m0, s36
	s_nop 0
	global_load_lds_dwordx4 v34, s[16:17] nt
	global_load_lds_dwordx4 v34, s[16:17] offset:1024 nt
	global_load_lds_dwordx4 v34, s[16:17] offset:2048 nt
	global_load_lds_dwordx4 v35, s[16:17] offset:3072 nt
	s_add_u32 s16, s16, 0x7d00
	s_addc_u32 s17, s17, 0
	v_cndmask_b32_e64 v30, 0, v30, s[18:19]
	v_cndmask_b32_e64 v31, 0, v31, s[18:19]
	v_cndmask_b32_e64 v32, 0, v32, s[18:19]
	v_cndmask_b32_e64 v33, 0, v33, s[18:19]
	v_max3_f32 v41, |v18|, |v19|, |v20|
	v_max3_f32 v42, |v21|, |v22|, |v23|
	v_max3_f32 v43, |v24|, |v25|, |v26|
	v_max3_f32 v44, |v27|, |v28|, |v29|
	v_max3_f32 v48, |v30|, |v31|, |v32|
	v_max3_f32 v41, v41, v42, |v33|
	v_max3_f32 v43, v43, v44, v48
	v_max_f32_e32 v41, v41, v43
	v_pk_add_f32 v[2:3], v[2:3], v[18:19]
	v_pk_add_f32 v[4:5], v[4:5], v[20:21]
	v_max_f32_dpp v41, v41, v41 quad_perm:[1,0,3,2] row_mask:0xf bank_mask:0xf
	v_pk_add_f32 v[6:7], v[6:7], v[22:23]
	v_pk_add_f32 v[8:9], v[8:9], v[24:25]
	v_max_f32_dpp v41, v41, v41 quad_perm:[2,3,0,1] row_mask:0xf bank_mask:0xf
	v_pk_add_f32 v[10:11], v[10:11], v[26:27]
	v_pk_add_f32 v[12:13], v[12:13], v[28:29]
	v_max_f32_dpp v41, v41, v41 row_half_mirror row_mask:0xf bank_mask:0xf
	v_pk_add_f32 v[14:15], v[14:15], v[30:31]
	v_pk_add_f32 v[16:17], v[16:17], v[32:33]
	v_max_f32_dpp v41, v41, v41 row_mirror row_mask:0xf bank_mask:0xf
	s_nop 1
	v_max_f32_dpp v41, v41, v41 row_bcast:15 row_mask:0xa bank_mask:0xf
	s_nop 1
	v_max_f32_dpp v41, v41, v41 row_bcast:31 row_mask:0xc bank_mask:0xf
	s_nop 1
	v_readlane_b32 s28, v41, 63
	s_nop 1
	v_div_scale_f32 v48, s[30:31], s28, s28, v47
	v_rcp_f32_e32 v49, v48
	s_nop 0
	v_fma_f32 v50, -v48, v49, 1.0
	v_fmac_f32_e32 v49, v50, v49
	v_mov_b32_e32 v50, s28
	v_div_scale_f32 v50, vcc, s32, v50, s32
	v_mul_f32_e32 v51, v50, v49
	v_fma_f32 v52, -v48, v51, v50
	v_fmac_f32_e32 v51, v52, v49
	v_fma_f32 v48, -v48, v51, v50
	v_div_fmas_f32 v48, v48, v49, v51
	v_div_fixup_f32 v48, v48, s28, v47
	v_cmp_gt_f32_e64 vcc, s28, 0
	v_writelane_b32 v40, s28, 21
	s_nop 0
	v_cndmask_b32_e32 v48, 0, v48, vcc
	v_fmaak_f32 v49, v18, v48, 0x4b400000
	v_fmaak_f32 v50, v19, v48, 0x4b400000
	v_fmaak_f32 v51, v20, v48, 0x4b400000
	v_fmaak_f32 v52, v21, v48, 0x4b400000
	v_perm_b32 v49, v50, v49, s33
	v_perm_b32 v51, v52, v51, s34
	v_or_b32_e32 v49, v49, v51
	s_add_u32 s20, s20, 0x400
	s_addc_u32 s21, s21, 0
	s_add_u32 s22, s22, 0x400
	s_addc_u32 s23, s23, 0
	s_add_u32 s24, s24, 0x400
	s_addc_u32 s25, s25, 0
	s_add_u32 s26, s26, 0x400
	s_addc_u32 s27, s27, 0
	global_store_dword v39, v49, s[20:21]
	v_fmaak_f32 v41, v22, v48, 0x4b400000
	v_fmaak_f32 v42, v23, v48, 0x4b400000
	v_fmaak_f32 v43, v24, v48, 0x4b400000
	v_fmaak_f32 v44, v25, v48, 0x4b400000
	v_perm_b32 v41, v42, v41, s33
	v_perm_b32 v43, v44, v43, s34
	v_or_b32_e32 v41, v41, v43
	global_store_dword v39, v41, s[22:23]
	v_fmaak_f32 v49, v26, v48, 0x4b400000
	v_fmaak_f32 v50, v27, v48, 0x4b400000
	v_fmaak_f32 v51, v28, v48, 0x4b400000
	v_fmaak_f32 v52, v29, v48, 0x4b400000
	v_perm_b32 v49, v50, v49, s33
	v_perm_b32 v51, v52, v51, s34
	v_or_b32_e32 v49, v49, v51
	global_store_dword v39, v49, s[24:25]
	v_fmaak_f32 v41, v30, v48, 0x4b400000
	v_fmaak_f32 v42, v31, v48, 0x4b400000
	v_fmaak_f32 v43, v32, v48, 0x4b400000
	v_fmaak_f32 v44, v33, v48, 0x4b400000
	v_perm_b32 v41, v42, v41, s33
	v_perm_b32 v43, v44, v43, s34
	v_or_b32_e32 v41, v41, v43
	global_store_dword v39, v41, s[26:27]
	s_waitcnt vmcnt(12)
	ds_read_b128 v[18:21], v38 offset:0
	ds_read_b128 v[22:25], v38 offset:1024
	ds_read_b128 v[26:29], v38 offset:2048
	ds_read_b128 v[30:33], v38 offset:3072
	s_waitcnt lgkmcnt(0)
	s_cmp_eq_u32 s29, 1
	s_cbranch_scc0 .Lk1_nodma24
	s_mov_b32 m0, s35
	s_nop 0
	global_load_lds_dwordx4 v34, s[16:17] nt
	global_load_lds_dwordx4 v34, s[16:17] offset:1024 nt
	global_load_lds_dwordx4 v34, s[16:17] offset:2048 nt
	global_load_lds_dwordx4 v35, s[16:17] offset:3072 nt
	s_add_u32 s16, s16, 0x7d00
	s_addc_u32 s17, s17, 0
.Lk1_nodma24:
	v_cndmask_b32_e64 v30, 0, v30, s[18:19]
	v_cndmask_b32_e64 v31, 0, v31, s[18:19]
	v_cndmask_b32_e64 v32, 0, v32, s[18:19]
	v_cndmask_b32_e64 v33, 0, v33, s[18:19]
	v_max3_f32 v41, |v18|, |v19|, |v20|
	v_max3_f32 v42, |v21|, |v22|, |v23|
	v_max3_f32 v43, |v24|, |v25|, |v26|
	v_max3_f32 v44, |v27|, |v28|, |v29|
	v_max3_f32 v48, |v30|, |v31|, |v32|
	v_max3_f32 v41, v41, v42, |v33|
	v_max3_f32 v43, v43, v44, v48
	v_max_f32_e32 v41, v41, v43
	v_pk_add_f32 v[2:3], v[2:3], v[18:19]
	v_pk_add_f32 v[4:5], v[4:5], v[20:21]
	v_max_f32_dpp v41, v41, v41 quad_perm:[1,0,3,2] row_mask:0xf bank_mask:0xf
	v_pk_add_f32 v[6:7], v[6:7], v[22:23]
	v_pk_add_f32 v[8:9], v[8:9], v[24:25]
	v_max_f32_dpp v41, v41, v41 quad_perm:[2,3,0,1] row_mask:0xf bank_mask:0xf
	v_pk_add_f32 v[10:11], v[10:11], v[26:27]
	v_pk_add_f32 v[12:13], v[12:13], v[28:29]
	v_max_f32_dpp v41, v41, v41 row_half_mirror row_mask:0xf bank_mask:0xf
	v_pk_add_f32 v[14:15], v[14:15], v[30:31]
	v_pk_add_f32 v[16:17], v[16:17], v[32:33]
	v_max_f32_dpp v41, v41, v41 row_mirror row_mask:0xf bank_mask:0xf
	s_nop 1
	v_max_f32_dpp v41, v41, v41 row_bcast:15 row_mask:0xa bank_mask:0xf
	s_nop 1
	v_max_f32_dpp v41, v41, v41 row_bcast:31 row_mask:0xc bank_mask:0xf
	s_nop 1
	v_readlane_b32 s28, v41, 63
	s_nop 1
	v_div_scale_f32 v48, s[30:31], s28, s28, v47
	v_rcp_f32_e32 v49, v48
	s_nop 0
	v_fma_f32 v50, -v48, v49, 1.0
	v_fmac_f32_e32 v49, v50, v49
	v_mov_b32_e32 v50, s28
	v_div_scale_f32 v50, vcc, s32, v50, s32
	v_mul_f32_e32 v51, v50, v49
	v_fma_f32 v52, -v48, v51, v50
	v_fmac_f32_e32 v51, v52, v49
	v_fma_f32 v48, -v48, v51, v50
	v_div_fmas_f32 v48, v48, v49, v51
	v_div_fixup_f32 v48, v48, s28, v47
	v_cmp_gt_f32_e64 vcc, s28, 0
	v_writelane_b32 v40, s28, 22
	s_nop 0
	v_cndmask_b32_e32 v48, 0, v48, vcc
	v_fmaak_f32 v49, v18, v48, 0x4b400000
	v_fmaak_f32 v50, v19, v48, 0x4b400000
	v_fmaak_f32 v51, v20, v48, 0x4b400000
	v_fmaak_f32 v52, v21, v48, 0x4b400000
	v_perm_b32 v49, v50, v49, s33
	v_perm_b32 v51, v52, v51, s34
	v_or_b32_e32 v49, v49, v51
	s_add_u32 s20, s20, 0x400
	s_addc_u32 s21, s21, 0
	s_add_u32 s22, s22, 0x400
	s_addc_u32 s23, s23, 0
	s_add_u32 s24, s24, 0x400
	s_addc_u32 s25, s25, 0
	s_add_u32 s26, s26, 0x400
	s_addc_u32 s27, s27, 0
	global_store_dword v39, v49, s[20:21]
	v_fmaak_f32 v41, v22, v48, 0x4b400000
	v_fmaak_f32 v42, v23, v48, 0x4b400000
	v_fmaak_f32 v43, v24, v48, 0x4b400000
	v_fmaak_f32 v44, v25, v48, 0x4b400000
	v_perm_b32 v41, v42, v41, s33
	v_perm_b32 v43, v44, v43, s34
	v_or_b32_e32 v41, v41, v43
	global_store_dword v39, v41, s[22:23]
	v_fmaak_f32 v49, v26, v48, 0x4b400000
	v_fmaak_f32 v50, v27, v48, 0x4b400000
	v_fmaak_f32 v51, v28, v48, 0x4b400000
	v_fmaak_f32 v52, v29, v48, 0x4b400000
	v_perm_b32 v49, v50, v49, s33
	v_perm_b32 v51, v52, v51, s34
	v_or_b32_e32 v49, v49, v51
	global_store_dword v39, v49, s[24:25]
	v_fmaak_f32 v41, v30, v48, 0x4b400000
	v_fmaak_f32 v42, v31, v48, 0x4b400000
	v_fmaak_f32 v43, v32, v48, 0x4b400000
	v_fmaak_f32 v44, v33, v48, 0x4b400000
	v_perm_b32 v41, v42, v41, s33
	v_perm_b32 v43, v44, v43, s34
	v_or_b32_e32 v41, v41, v43
	global_store_dword v39, v41, s[26:27]
	s_waitcnt vmcnt(8)
	ds_read_b128 v[18:21], v38 offset:4096
	ds_read_b128 v[22:25], v38 offset:5120
	ds_read_b128 v[26:29], v38 offset:6144
	ds_read_b128 v[30:33], v38 offset:7168
	s_waitcnt lgkmcnt(0)
	v_cndmask_b32_e64 v30, 0, v30, s[18:19]
	v_cndmask_b32_e64 v31, 0, v31, s[18:19]
	v_cndmask_b32_e64 v32, 0, v32, s[18:19]
	v_cndmask_b32_e64 v33, 0, v33, s[18:19]
	v_max3_f32 v41, |v18|, |v19|, |v20|
	v_max3_f32 v42, |v21|, |v22|, |v23|
	v_max3_f32 v43, |v24|, |v25|, |v26|
	v_max3_f32 v44, |v27|, |v28|, |v29|
	v_max3_f32 v48, |v30|, |v31|, |v32|
	v_max3_f32 v41, v41, v42, |v33|
	v_max3_f32 v43, v43, v44, v48
	v_max_f32_e32 v41, v41, v43
	v_pk_add_f32 v[2:3], v[2:3], v[18:19]
	v_pk_add_f32 v[4:5], v[4:5], v[20:21]
	v_max_f32_dpp v41, v41, v41 quad_perm:[1,0,3,2] row_mask:0xf bank_mask:0xf
	v_pk_add_f32 v[6:7], v[6:7], v[22:23]
	v_pk_add_f32 v[8:9], v[8:9], v[24:25]
	v_max_f32_dpp v41, v41, v41 quad_perm:[2,3,0,1] row_mask:0xf bank_mask:0xf
	v_pk_add_f32 v[10:11], v[10:11], v[26:27]
	v_pk_add_f32 v[12:13], v[12:13], v[28:29]
	v_max_f32_dpp v41, v41, v41 row_half_mirror row_mask:0xf bank_mask:0xf
	v_pk_add_f32 v[14:15], v[14:15], v[30:31]
	v_pk_add_f32 v[16:17], v[16:17], v[32:33]
	v_max_f32_dpp v41, v41, v41 row_mirror row_mask:0xf bank_mask:0xf
	s_nop 1
	v_max_f32_dpp v41, v41, v41 row_bcast:15 row_mask:0xa bank_mask:0xf
	s_nop 1
	v_max_f32_dpp v41, v41, v41 row_bcast:31 row_mask:0xc bank_mask:0xf
	s_nop 1
	v_readlane_b32 s28, v41, 63
	s_nop 1
	v_div_scale_f32 v48, s[30:31], s28, s28, v47
	v_rcp_f32_e32 v49, v48
	s_nop 0
	v_fma_f32 v50, -v48, v49, 1.0
	v_fmac_f32_e32 v49, v50, v49
	v_mov_b32_e32 v50, s28
	v_div_scale_f32 v50, vcc, s32, v50, s32
	v_mul_f32_e32 v51, v50, v49
	v_fma_f32 v52, -v48, v51, v50
	v_fmac_f32_e32 v51, v52, v49
	v_fma_f32 v48, -v48, v51, v50
	v_div_fmas_f32 v48, v48, v49, v51
	v_div_fixup_f32 v48, v48, s28, v47
	v_cmp_gt_f32_e64 vcc, s28, 0
	v_writelane_b32 v40, s28, 23
	s_nop 0
	v_cndmask_b32_e32 v48, 0, v48, vcc
	v_fmaak_f32 v49, v18, v48, 0x4b400000
	v_fmaak_f32 v50, v19, v48, 0x4b400000
	v_fmaak_f32 v51, v20, v48, 0x4b400000
	v_fmaak_f32 v52, v21, v48, 0x4b400000
	v_perm_b32 v49, v50, v49, s33
	v_perm_b32 v51, v52, v51, s34
	v_or_b32_e32 v49, v49, v51
	s_add_u32 s20, s20, 0x400
	s_addc_u32 s21, s21, 0
	s_add_u32 s22, s22, 0x400
	s_addc_u32 s23, s23, 0
	s_add_u32 s24, s24, 0x400
	s_addc_u32 s25, s25, 0
	s_add_u32 s26, s26, 0x400
	s_addc_u32 s27, s27, 0
	global_store_dword v39, v49, s[20:21]
	v_fmaak_f32 v41, v22, v48, 0x4b400000
	v_fmaak_f32 v42, v23, v48, 0x4b400000
	v_fmaak_f32 v43, v24, v48, 0x4b400000
	v_fmaak_f32 v44, v25, v48, 0x4b400000
	v_perm_b32 v41, v42, v41, s33
	v_perm_b32 v43, v44, v43, s34
	v_or_b32_e32 v41, v41, v43
	global_store_dword v39, v41, s[22:23]
	v_fmaak_f32 v49, v26, v48, 0x4b400000
	v_fmaak_f32 v50, v27, v48, 0x4b400000
	v_fmaak_f32 v51, v28, v48, 0x4b400000
	v_fmaak_f32 v52, v29, v48, 0x4b400000
	v_perm_b32 v49, v50, v49, s33
	v_perm_b32 v51, v52, v51, s34
	v_or_b32_e32 v49, v49, v51
	global_store_dword v39, v49, s[24:25]
	v_fmaak_f32 v41, v30, v48, 0x4b400000
	v_fmaak_f32 v42, v31, v48, 0x4b400000
	v_fmaak_f32 v43, v32, v48, 0x4b400000
	v_fmaak_f32 v44, v33, v48, 0x4b400000
	v_perm_b32 v41, v42, v41, s33
	v_perm_b32 v43, v44, v43, s34
	v_or_b32_e32 v41, v41, v43
	global_store_dword v39, v41, s[26:27]
	s_cmp_eq_u32 s29, 1
	s_cbranch_scc0 .Lk1_flush
	s_waitcnt vmcnt(8)
	ds_read_b128 v[18:21], v38 offset:0
	ds_read_b128 v[22:25], v38 offset:1024
	ds_read_b128 v[26:29], v38 offset:2048
	ds_read_b128 v[30:33], v38 offset:3072
	s_waitcnt lgkmcnt(0)
	v_cndmask_b32_e64 v30, 0, v30, s[18:19]
	v_cndmask_b32_e64 v31, 0, v31, s[18:19]
	v_cndmask_b32_e64 v32, 0, v32, s[18:19]
	v_cndmask_b32_e64 v33, 0, v33, s[18:19]
	v_max3_f32 v41, |v18|, |v19|, |v20|
	v_max3_f32 v42, |v21|, |v22|, |v23|
	v_max3_f32 v43, |v24|, |v25|, |v26|
	v_max3_f32 v44, |v27|, |v28|, |v29|
	v_max3_f32 v48, |v30|, |v31|, |v32|
	v_max3_f32 v41, v41, v42, |v33|
	v_max3_f32 v43, v43, v44, v48
	v_max_f32_e32 v41, v41, v43
	v_pk_add_f32 v[2:3], v[2:3], v[18:19]
	v_pk_add_f32 v[4:5], v[4:5], v[20:21]
	v_max_f32_dpp v41, v41, v41 quad_perm:[1,0,3,2] row_mask:0xf bank_mask:0xf
	v_pk_add_f32 v[6:7], v[6:7], v[22:23]
	v_pk_add_f32 v[8:9], v[8:9], v[24:25]
	v_max_f32_dpp v41, v41, v41 quad_perm:[2,3,0,1] row_mask:0xf bank_mask:0xf
	v_pk_add_f32 v[10:11], v[10:11], v[26:27]
	v_pk_add_f32 v[12:13], v[12:13], v[28:29]
	v_max_f32_dpp v41, v41, v41 row_half_mirror row_mask:0xf bank_mask:0xf
	v_pk_add_f32 v[14:15], v[14:15], v[30:31]
	v_pk_add_f32 v[16:17], v[16:17], v[32:33]
	v_max_f32_dpp v41, v41, v41 row_mirror row_mask:0xf bank_mask:0xf
	s_nop 1
	v_max_f32_dpp v41, v41, v41 row_bcast:15 row_mask:0xa bank_mask:0xf
	s_nop 1
	v_max_f32_dpp v41, v41, v41 row_bcast:31 row_mask:0xc bank_mask:0xf
	s_nop 1
	v_readlane_b32 s28, v41, 63
	s_nop 1
	v_div_scale_f32 v48, s[30:31], s28, s28, v47
	v_rcp_f32_e32 v49, v48
	s_nop 0
	v_fma_f32 v50, -v48, v49, 1.0
	v_fmac_f32_e32 v49, v50, v49
	v_mov_b32_e32 v50, s28
	v_div_scale_f32 v50, vcc, s32, v50, s32
	v_mul_f32_e32 v51, v50, v49
	v_fma_f32 v52, -v48, v51, v50
	v_fmac_f32_e32 v51, v52, v49
	v_fma_f32 v48, -v48, v51, v50
	v_div_fmas_f32 v48, v48, v49, v51
	v_div_fixup_f32 v48, v48, s28, v47
	v_cmp_gt_f32_e64 vcc, s28, 0
	v_writelane_b32 v40, s28, 24
	s_nop 0
	v_cndmask_b32_e32 v48, 0, v48, vcc
	v_fmaak_f32 v49, v18, v48, 0x4b400000
	v_fmaak_f32 v50, v19, v48, 0x4b400000
	v_fmaak_f32 v51, v20, v48, 0x4b400000
	v_fmaak_f32 v52, v21, v48, 0x4b400000
	v_perm_b32 v49, v50, v49, s33
	v_perm_b32 v51, v52, v51, s34
	v_or_b32_e32 v49, v49, v51
	s_add_u32 s20, s20, 0x400
	s_addc_u32 s21, s21, 0
	s_add_u32 s22, s22, 0x400
	s_addc_u32 s23, s23, 0
	s_add_u32 s24, s24, 0x400
	s_addc_u32 s25, s25, 0
	s_add_u32 s26, s26, 0x400
	s_addc_u32 s27, s27, 0
	global_store_dword v39, v49, s[20:21]
	v_fmaak_f32 v41, v22, v48, 0x4b400000
	v_fmaak_f32 v42, v23, v48, 0x4b400000
	v_fmaak_f32 v43, v24, v48, 0x4b400000
	v_fmaak_f32 v44, v25, v48, 0x4b400000
	v_perm_b32 v41, v42, v41, s33
	v_perm_b32 v43, v44, v43, s34
	v_or_b32_e32 v41, v41, v43
	global_store_dword v39, v41, s[22:23]
	v_fmaak_f32 v49, v26, v48, 0x4b400000
	v_fmaak_f32 v50, v27, v48, 0x4b400000
	v_fmaak_f32 v51, v28, v48, 0x4b400000
	v_fmaak_f32 v52, v29, v48, 0x4b400000
	v_perm_b32 v49, v50, v49, s33
	v_perm_b32 v51, v52, v51, s34
	v_or_b32_e32 v49, v49, v51
	global_store_dword v39, v49, s[24:25]
	v_fmaak_f32 v41, v30, v48, 0x4b400000
	v_fmaak_f32 v42, v31, v48, 0x4b400000
	v_fmaak_f32 v43, v32, v48, 0x4b400000
	v_fmaak_f32 v44, v33, v48, 0x4b400000
	v_perm_b32 v41, v42, v41, s33
	v_perm_b32 v43, v44, v43, s34
	v_or_b32_e32 v41, v41, v43
	global_store_dword v39, v41, s[26:27]
.Lk1_flush:
	s_add_u32 s20, s40, 0x0
	s_addc_u32 s21, s41, 0
	s_add_u32 s22, s20, 0x186a000
	s_addc_u32 s23, s21, 0
	s_add_u32 s24, s22, 0x186a000
	s_addc_u32 s25, s23, 0
	s_add_u32 s26, s24, 0x186a000
	s_addc_u32 s27, s25, 0
	global_store_dword v39, v56, s[20:21] sc1
	global_store_dword v39, v57, s[22:23] sc1
	global_store_dword v39, v58, s[24:25] sc1
	global_store_dword v39, v59, s[26:27] sc1
	global_store_dword v39, v60, s[20:21] offset:1024 sc1
	global_store_dword v39, v61, s[22:23] offset:1024 sc1
	global_store_dword v39, v62, s[24:25] offset:1024 sc1
	global_store_dword v39, v63, s[26:27] offset:1024 sc1
	global_store_dword v39, v64, s[20:21] offset:2048 sc1
	global_store_dword v39, v65, s[22:23] offset:2048 sc1
	global_store_dword v39, v66, s[24:25] offset:2048 sc1
	global_store_dword v39, v67, s[26:27] offset:2048 sc1
	global_store_dword v39, v68, s[20:21] offset:3072 sc1
	global_store_dword v39, v69, s[22:23] offset:3072 sc1
	global_store_dword v39, v70, s[24:25] offset:3072 sc1
	global_store_dword v39, v71, s[26:27] offset:3072 sc1
	s_add_u32 s20, s20, 0x1000
	s_addc_u32 s21, s21, 0
	s_add_u32 s22, s22, 0x1000
	s_addc_u32 s23, s23, 0
	s_add_u32 s24, s24, 0x1000
	s_addc_u32 s25, s25, 0
	s_add_u32 s26, s26, 0x1000
	s_addc_u32 s27, s27, 0
	global_store_dword v39, v72, s[20:21] sc1
	global_store_dword v39, v73, s[22:23] sc1
	global_store_dword v39, v74, s[24:25] sc1
	global_store_dword v39, v75, s[26:27] sc1
	global_store_dword v39, v76, s[20:21] offset:1024 sc1
	global_store_dword v39, v77, s[22:23] offset:1024 sc1
	global_store_dword v39, v78, s[24:25] offset:1024 sc1
	global_store_dword v39, v79, s[26:27] offset:1024 sc1
	global_store_dword v39, v80, s[20:21] offset:2048 sc1
	global_store_dword v39, v81, s[22:23] offset:2048 sc1
	global_store_dword v39, v82, s[24:25] offset:2048 sc1
	global_store_dword v39, v83, s[26:27] offset:2048 sc1
	global_store_dword v39, v84, s[20:21] offset:3072 sc1
	global_store_dword v39, v85, s[22:23] offset:3072 sc1
	global_store_dword v39, v86, s[24:25] offset:3072 sc1
	global_store_dword v39, v87, s[26:27] offset:3072 sc1
	s_add_u32 s20, s20, 0x1000
	s_addc_u32 s21, s21, 0
	s_add_u32 s22, s22, 0x1000
	s_addc_u32 s23, s23, 0
	s_add_u32 s24, s24, 0x1000
	s_addc_u32 s25, s25, 0
	s_add_u32 s26, s26, 0x1000
	s_addc_u32 s27, s27, 0
	global_store_dword v39, v88, s[20:21] sc1
	global_store_dword v39, v89, s[22:23] sc1
	global_store_dword v39, v90, s[24:25] sc1
	global_store_dword v39, v91, s[26:27] sc1
	global_store_dword v39, v92, s[20:21] offset:1024 sc1
	global_store_dword v39, v93, s[22:23] offset:1024 sc1
	global_store_dword v39, v94, s[24:25] offset:1024 sc1
	global_store_dword v39, v95, s[26:27] offset:1024 sc1
	global_store_dword v39, v96, s[20:21] offset:2048 sc1
	global_store_dword v39, v97, s[22:23] offset:2048 sc1
	global_store_dword v39, v98, s[24:25] offset:2048 sc1
	global_store_dword v39, v99, s[26:27] offset:2048 sc1
	global_store_dword v39, v100, s[20:21] offset:3072 sc1
	global_store_dword v39, v101, s[22:23] offset:3072 sc1
	global_store_dword v39, v102, s[24:25] offset:3072 sc1
	global_store_dword v39, v103, s[26:27] offset:3072 sc1
	s_add_u32 s20, s20, 0x1000
	s_addc_u32 s21, s21, 0
	s_add_u32 s22, s22, 0x1000
	s_addc_u32 s23, s23, 0
	s_add_u32 s24, s24, 0x1000
	s_addc_u32 s25, s25, 0
	s_add_u32 s26, s26, 0x1000
	s_addc_u32 s27, s27, 0
	global_store_dword v39, v104, s[20:21] sc1
	global_store_dword v39, v105, s[22:23] sc1
	global_store_dword v39, v106, s[24:25] sc1
	global_store_dword v39, v107, s[26:27] sc1
	global_store_dword v39, v108, s[20:21] offset:1024 sc1
	global_store_dword v39, v109, s[22:23] offset:1024 sc1
	global_store_dword v39, v110, s[24:25] offset:1024 sc1
	global_store_dword v39, v111, s[26:27] offset:1024 sc1
	global_store_dword v39, v112, s[20:21] offset:2048 sc1
	global_store_dword v39, v113, s[22:23] offset:2048 sc1
	global_store_dword v39, v114, s[24:25] offset:2048 sc1
	global_store_dword v39, v115, s[26:27] offset:2048 sc1
	global_store_dword v39, v116, s[20:21] offset:3072 sc1
	global_store_dword v39, v117, s[22:23] offset:3072 sc1
	global_store_dword v39, v118, s[24:25] offset:3072 sc1
	global_store_dword v39, v119, s[26:27] offset:3072 sc1
	s_add_u32 s20, s20, 0x1000
	s_addc_u32 s21, s21, 0
	s_add_u32 s22, s22, 0x1000
	s_addc_u32 s23, s23, 0
	s_add_u32 s24, s24, 0x1000
	s_addc_u32 s25, s25, 0
	s_add_u32 s26, s26, 0x1000
	s_addc_u32 s27, s27, 0
	global_store_dword v39, v120, s[20:21] sc1
	global_store_dword v39, v121, s[22:23] sc1
	global_store_dword v39, v122, s[24:25] sc1
	global_store_dword v39, v123, s[26:27] sc1
	global_store_dword v39, v124, s[20:21] offset:1024 sc1
	global_store_dword v39, v125, s[22:23] offset:1024 sc1
	global_store_dword v39, v126, s[24:25] offset:1024 sc1
	global_store_dword v39, v127, s[26:27] offset:1024 sc1
	v_mul_f32_e32 v40, 0x3c010204, v40
	v_and_b32_e32 v42, 63, v0
	v_lshlrev_b32_e32 v41, 5, v42
	s_add_u32 s15, s12, s14
	s_lshl_b32 s15, s15, 2
	s_add_u32 s8, s8, s15
	s_addc_u32 s9, s9, 0
	s_add_u32 s15, s29, 24
	v_cmp_gt_u32_e32 vcc, s15, v42
	s_and_saveexec_b64 s[38:39], vcc
	global_store_dword v41, v40, s[8:9]
	s_mov_b64 exec, s[38:39]
	s_lshl_b32 s15, s14, 12
	v_add_u32_e32 v41, s15, v34
	s_barrier
	ds_write_b128 v41, v[2:5]
	ds_write_b128 v41, v[6:9] offset:1024
	ds_write_b128 v41, v[10:13] offset:2048
	ds_write_b128 v41, v[14:17] offset:3072
	s_waitcnt lgkmcnt(0)
	s_barrier
	s_movk_i32 s15, 0x100
	v_cmp_gt_u32_e32 vcc, s15, v0
	s_and_saveexec_b64 s[38:39], vcc
	s_cbranch_execz .Lk1_end
	v_lshlrev_b32_e32 v16, 4, v0
	ds_read_b128 v[2:5], v16
	ds_read_b128 v[18:21], v16 offset:4096
	ds_read_b128 v[22:25], v16 offset:8192
	ds_read_b128 v[26:29], v16 offset:12288
	ds_read_b128 v[30:33], v16 offset:16384
	ds_read_b128 v[34:37], v16 offset:20480
	ds_read_b128 v[38:41], v16 offset:24576
	ds_read_b128 v[42:45], v16 offset:28672
	s_waitcnt lgkmcnt(6)
	v_pk_add_f32 v[2:3], v[2:3], v[18:19]
	v_pk_add_f32 v[4:5], v[4:5], v[20:21]
	s_waitcnt lgkmcnt(5)
	v_pk_add_f32 v[2:3], v[2:3], v[22:23]
	v_pk_add_f32 v[4:5], v[4:5], v[24:25]
	s_waitcnt lgkmcnt(4)
	v_pk_add_f32 v[2:3], v[2:3], v[26:27]
	v_pk_add_f32 v[4:5], v[4:5], v[28:29]
	s_waitcnt lgkmcnt(3)
	v_pk_add_f32 v[2:3], v[2:3], v[30:31]
	v_pk_add_f32 v[4:5], v[4:5], v[32:33]
	s_waitcnt lgkmcnt(2)
	v_pk_add_f32 v[2:3], v[2:3], v[34:35]
	v_pk_add_f32 v[4:5], v[4:5], v[36:37]
	s_waitcnt lgkmcnt(1)
	v_pk_add_f32 v[2:3], v[2:3], v[38:39]
	v_pk_add_f32 v[4:5], v[4:5], v[40:41]
	s_waitcnt lgkmcnt(0)
	v_pk_add_f32 v[2:3], v[2:3], v[42:43]
	v_pk_add_f32 v[4:5], v[4:5], v[44:45]
	s_lshl_b32 s15, s2, 12
	s_add_u32 s10, s10, s15
	s_addc_u32 s11, s11, 0
	global_store_dwordx4 v16, v[2:5], s[10:11]
